# P3 filter tile: layer biases and sine frequencies preloaded at tile start (no exposed per-unit global loads)
# speedup vs baseline: 1.0052x; 1.0028x over previous
.LBB0_372:
	v_mov_b64_e32 v[2:3], v[122:123]
	global_load_dword v5, v[2:3], off
	global_load_dword v208, v[2:3], off offset:2048
	v_lshl_add_u64 v[2:3], v[2:3], 0, s[28:29]
	v_lshl_add_u64 v[2:3], v[2:3], 0, s[28:29]
	global_load_dword v209, v[2:3], off
	global_load_dword v210, v[2:3], off offset:2048
	v_lshl_add_u64 v[2:3], v[2:3], 0, s[28:29]
	v_lshl_add_u64 v[2:3], v[2:3], 0, s[28:29]
	v_add_u32_e32 v1, 0x800, v139
	v_cmp_ge_u32_e32 vcc, s33, v1
	s_and_saveexec_b64 s[6:7], vcc
	global_load_dword v211, v[2:3], off
	s_mov_b64 exec, s[6:7]
	global_load_dwordx4 v[220:223], v[64:65], off
	global_load_dwordx4 v[224:227], v[64:65], off offset:16
	global_load_dwordx4 v[228:231], v[66:67], off
	global_load_dwordx4 v[232:235], v[66:67], off offset:16
	global_load_dwordx4 v[236:239], v[68:69], off
	global_load_dwordx4 v[240:243], v[68:69], off offset:16
	global_load_dwordx4 v[244:247], v[70:71], off
	global_load_dwordx4 v[248:251], v[70:71], off offset:16
	s_waitcnt vmcnt(0)
	ds_write_b32 v138, v5
	ds_write_b32 v138, v208 offset:2048
	ds_write_b32 v138, v209 offset:4096
	ds_write_b32 v138, v210 offset:6144
	s_and_saveexec_b64 s[6:7], vcc
	ds_write_b32 v138, v211 offset:8192
	s_mov_b64 exec, s[6:7]
	global_load_dword v1, v[108:109], off
	global_load_dword v2, v[108:109], off offset:2048
	global_load_dword v3, v[110:111], off
	global_load_dword v4, v[112:113], off
	global_load_dword v5, v[114:115], off
	global_load_dword v6, v[116:117], off
	global_load_dword v7, v[118:119], off
	s_waitcnt vmcnt(5)
	ds_write2st64_b32 v137, v1, v2 offset0:198 offset1:206
	s_waitcnt vmcnt(3)
	ds_write2st64_b32 v137, v3, v4 offset0:214 offset1:222
	s_waitcnt vmcnt(1)
	ds_write2st64_b32 v137, v5, v6 offset0:230 offset1:238
	s_waitcnt vmcnt(0)
	ds_write_b32 v137, v7 offset:62976
	s_and_saveexec_b64 s[6:7], s[4:5]
	s_xor_b64 s[6:7], exec, s[6:7]
	s_cbranch_execz .LBB0_376
	global_load_dword v1, v[120:121], off
	s_waitcnt vmcnt(0)
	ds_write_b32 v137, v1 offset:65024

.LBB0_392:
	s_andn2_saveexec_b64 s[6:7], s[34:35]
	v_cvt_i32_f32_e32 v6, v5
	v_fma_f32 v7, v5, s47, |v1|
	v_fmac_f32_e32 v7, 0xb3a22168, v5
	v_fmac_f32_e32 v7, 0xa7c234c4, v5
	s_or_b64 exec, exec, s[6:7]
	v_mul_f32_e32 v3, v7, v7
	v_fmamk_f32 v4, v3, 0xb94c1982, v125
	v_fmaak_f32 v4, v3, v4, 0xbe2aaa9d
	v_mul_f32_e32 v4, v3, v4
	v_fmac_f32_e32 v7, v7, v4
	v_fmamk_f32 v4, v3, 0x37d75334, v143
	v_fmaak_f32 v4, v3, v4, 0x3d2aabf7
	v_fmaak_f32 v4, v3, v4, 0xbf000004
	v_fma_f32 v3, v3, v4, 1.0
	v_and_b32_e32 v4, 1, v6
	v_cmp_eq_u32_e64 s[6:7], 0, v4
	v_lshlrev_b32_e32 v4, 30, v6
	v_and_b32_e32 v4, 0x80000000, v4
	v_xor_b32_e32 v1, v2, v1
	v_cndmask_b32_e64 v3, v3, v7, s[6:7]
	v_xor_b32_e32 v1, v1, v4
	v_xor_b32_e32 v1, v1, v3
	v_cndmask_b32_e64 v1, v148, -v1, vcc
	ds_write_b32 v136, v1 offset:72
	s_waitcnt lgkmcnt(0)
	s_barrier
	v_mov_b64_e32 v[6:7], v[220:221]
	v_mov_b64_e32 v[8:9], v[222:223]
	v_mov_b64_e32 v[2:3], v[224:225]
	v_mov_b64_e32 v[4:5], v[226:227]
	s_mov_b32 s6, 0
	v_mov_b32_e32 v1, v140
	v_add_u32_e32 v14, s6, v17
	ds_read_b128 v[10:13], v1
	ds_read_b128 v[18:21], v1 offset:16
	ds_read_b32 v14, v14
	s_add_i32 s6, s6, 4
	v_add_u32_e32 v1, 0x100, v1
.LBB0_395:
	v_add_u32_e32 v216, s6, v17
	ds_read_b128 v[208:211], v1
	ds_read_b128 v[212:215], v1 offset:16
	ds_read_b32 v216, v216
	s_add_i32 s6, s6, 4
	v_add_u32_e32 v1, 0x100, v1
	s_waitcnt vmcnt(0) lgkmcnt(3)
	v_pk_fma_f32 v[6:7], v[14:15], v[10:11], v[6:7] op_sel_hi:[0,1,1]
	v_pk_fma_f32 v[8:9], v[14:15], v[12:13], v[8:9] op_sel_hi:[0,1,1]
	v_pk_fma_f32 v[2:3], v[14:15], v[18:19], v[2:3] op_sel_hi:[0,1,1]
	v_pk_fma_f32 v[4:5], v[14:15], v[20:21], v[4:5] op_sel_hi:[0,1,1]
	v_add_u32_e32 v14, s6, v17
	ds_read_b128 v[10:13], v1
	ds_read_b128 v[18:21], v1 offset:16
	ds_read_b32 v14, v14
	s_add_i32 s6, s6, 4
	v_add_u32_e32 v1, 0x100, v1
	s_waitcnt lgkmcnt(3)
	v_pk_fma_f32 v[6:7], v[216:217], v[208:209], v[6:7] op_sel_hi:[0,1,1]
	v_pk_fma_f32 v[8:9], v[216:217], v[210:211], v[8:9] op_sel_hi:[0,1,1]
	v_pk_fma_f32 v[2:3], v[216:217], v[212:213], v[2:3] op_sel_hi:[0,1,1]
	v_pk_fma_f32 v[4:5], v[216:217], v[214:215], v[4:5] op_sel_hi:[0,1,1]
	s_cmpk_eq_i32 s6, 0x84
	s_cbranch_scc0 .LBB0_395
	s_waitcnt lgkmcnt(0)
	v_pk_fma_f32 v[6:7], v[14:15], v[10:11], v[6:7] op_sel_hi:[0,1,1]
	v_pk_fma_f32 v[8:9], v[14:15], v[12:13], v[8:9] op_sel_hi:[0,1,1]
	v_pk_fma_f32 v[2:3], v[14:15], v[18:19], v[2:3] op_sel_hi:[0,1,1]
	v_pk_fma_f32 v[4:5], v[14:15], v[20:21], v[4:5] op_sel_hi:[0,1,1]
	v_mov_b32_e32 v1, v228
	s_waitcnt vmcnt(0)
	v_mul_f32_e32 v1, v6, v1
	v_and_b32_e32 v6, 0x7fffffff, v1
	v_cmp_nlt_f32_e64 s[6:7], |v1|, s37
	s_and_saveexec_b64 s[8:9], s[6:7]
	s_xor_b64 s[12:13], exec, s[8:9]
	s_cbranch_execz .LBB0_398
	v_lshrrev_b32_e32 v10, 23, v6
	v_add_u32_e32 v10, 0xffffff88, v10
	v_cmp_lt_u32_e32 vcc, 63, v10
	s_nop 1
	v_cndmask_b32_e32 v11, 0, v145, vcc
	v_add_u32_e32 v10, v11, v10
	v_cmp_lt_u32_e64 s[6:7], 31, v10
	s_nop 1
	v_cndmask_b32_e64 v11, 0, v146, s[6:7]
	v_add_u32_e32 v10, v11, v10
	v_cmp_lt_u32_e64 s[8:9], 31, v10
	s_nop 1
	v_cndmask_b32_e64 v11, 0, v146, s[8:9]
	v_add_u32_e32 v16, v11, v10
	v_and_b32_e32 v10, 0x7fffff, v6
	v_or_b32_e32 v24, 0x800000, v10
	v_mad_u64_u32 v[10:11], s[10:11], v24, s38, 0
	v_mov_b32_e32 v62, v11
	v_mad_u64_u32 v[12:13], s[10:11], v24, s39, v[62:63]
	v_mov_b32_e32 v62, v13
	v_mad_u64_u32 v[14:15], s[10:11], v24, s40, v[62:63]
	v_mov_b32_e32 v62, v15
	v_mad_u64_u32 v[18:19], s[10:11], v24, s41, v[62:63]
	v_mov_b32_e32 v62, v19
	v_mad_u64_u32 v[20:21], s[10:11], v24, s42, v[62:63]
	v_mov_b32_e32 v62, v21
	v_mad_u64_u32 v[22:23], s[10:11], v24, s43, v[62:63]
	v_mov_b32_e32 v62, v23
	v_mad_u64_u32 v[24:25], s[10:11], v24, s44, v[62:63]
	v_cndmask_b32_e32 v11, v22, v18, vcc
	v_cndmask_b32_e32 v13, v24, v20, vcc
	v_cndmask_b32_e32 v19, v25, v22, vcc
	v_cndmask_b32_e64 v15, v13, v11, s[6:7]
	v_cndmask_b32_e64 v13, v19, v13, s[6:7]
	v_cndmask_b32_e32 v19, v20, v14, vcc
	v_cndmask_b32_e64 v11, v11, v19, s[6:7]
	v_cndmask_b32_e32 v12, v18, v12, vcc
	v_cndmask_b32_e64 v13, v13, v15, s[8:9]
	v_cndmask_b32_e64 v15, v15, v11, s[8:9]
	v_sub_u32_e32 v20, 32, v16
	v_cmp_eq_u32_e64 s[10:11], 0, v16
	v_cndmask_b32_e64 v16, v19, v12, s[6:7]
	v_alignbit_b32 v21, v13, v15, v20
	v_cndmask_b32_e64 v11, v11, v16, s[8:9]
	v_cndmask_b32_e64 v13, v21, v13, s[10:11]
	v_alignbit_b32 v18, v15, v11, v20
	v_cndmask_b32_e32 v10, v14, v10, vcc
	v_cndmask_b32_e64 v15, v18, v15, s[10:11]
	v_bfe_u32 v21, v13, 29, 1
	v_cndmask_b32_e64 v10, v12, v10, s[6:7]
	v_alignbit_b32 v18, v13, v15, 30
	v_sub_u32_e32 v22, 0, v21
	v_cndmask_b32_e64 v10, v16, v10, s[8:9]
	v_xor_b32_e32 v18, v18, v22
	v_alignbit_b32 v12, v11, v10, v20
	v_cndmask_b32_e64 v11, v12, v11, s[10:11]
	v_ffbh_u32_e32 v14, v18
	v_alignbit_b32 v12, v15, v11, 30
	v_min_u32_e32 v14, 32, v14
	v_alignbit_b32 v10, v11, v10, 30
	v_xor_b32_e32 v12, v12, v22
	v_sub_u32_e32 v15, 31, v14
	v_xor_b32_e32 v10, v10, v22
	v_alignbit_b32 v16, v18, v12, v15
	v_alignbit_b32 v10, v12, v10, v15
	v_alignbit_b32 v11, v16, v10, 9
	v_ffbh_u32_e32 v12, v11
	v_min_u32_e32 v12, 32, v12
	v_lshrrev_b32_e32 v19, 29, v13
	v_not_b32_e32 v15, v12
	v_alignbit_b32 v10, v11, v10, v15
	v_lshlrev_b32_e32 v11, 31, v19
	v_or_b32_e32 v15, 0x33000000, v11
	v_add_lshl_u32 v12, v12, v14, 23
	v_lshrrev_b32_e32 v10, 9, v10
	v_sub_u32_e32 v12, v15, v12
	v_or_b32_e32 v11, 0.5, v11
	v_lshlrev_b32_e32 v14, 23, v14
	v_or_b32_e32 v10, v12, v10
	v_lshrrev_b32_e32 v12, 9, v16
	v_sub_u32_e32 v11, v11, v14
	v_or_b32_e32 v11, v12, v11
	v_mul_f32_e32 v12, 0x3fc90fda, v11
	v_fma_f32 v14, v11, s45, -v12
	v_fmac_f32_e32 v14, 0x33a22168, v11
	v_fmac_f32_e32 v14, 0x3fc90fda, v10
	v_lshrrev_b32_e32 v11, 30, v13
	v_add_f32_e32 v10, v12, v14
	v_add_u32_e32 v11, v21, v11
.LBB0_398:
	s_andn2_saveexec_b64 s[6:7], s[12:13]
	v_mul_f32_e64 v10, |v1|, s46
	v_rndne_f32_e32 v12, v10
	v_cvt_i32_f32_e32 v11, v12
	v_fma_f32 v10, v12, s47, |v1|
	v_fmac_f32_e32 v10, 0xb3a22168, v12
	v_fmac_f32_e32 v10, 0xa7c234c4, v12
	s_or_b64 exec, exec, s[6:7]
	v_mov_b32_e32 v12, v229
	v_mul_f32_e32 v13, v10, v10
	v_and_b32_e32 v14, 1, v11
	v_lshlrev_b32_e32 v11, 30, v11
	v_fmamk_f32 v15, v13, 0xb94c1982, v125
	v_fmamk_f32 v16, v13, 0x37d75334, v143
	v_xor_b32_e32 v6, v6, v1
	v_and_b32_e32 v11, 0x80000000, v11
	v_fmaak_f32 v15, v13, v15, 0xbe2aaa9d
	v_fmaak_f32 v16, v13, v16, 0x3d2aabf7
	v_xor_b32_e32 v6, v6, v11
	v_mul_f32_e32 v11, v13, v15
	v_fmaak_f32 v15, v13, v16, 0xbf000004
	v_fmac_f32_e32 v10, v10, v11
	v_fma_f32 v11, v13, v15, 1.0
	v_cmp_eq_u32_e32 vcc, 0, v14
	s_nop 1
	v_cndmask_b32_e32 v10, v11, v10, vcc
	v_xor_b32_e32 v6, v6, v10
	v_cmp_class_f32_e64 vcc, v1, s49
	s_nop 1
	v_cndmask_b32_e32 v1, v147, v6, vcc
	ds_write_b32 v133, v1 offset:9216
	s_waitcnt vmcnt(0)
	v_mul_f32_e32 v1, v7, v12
	v_and_b32_e32 v6, 0x7fffffff, v1
	v_cmp_nlt_f32_e64 s[6:7], |v1|, s37
	s_and_saveexec_b64 s[8:9], s[6:7]
	s_xor_b64 s[12:13], exec, s[8:9]
	s_cbranch_execz .LBB0_402
	v_lshrrev_b32_e32 v7, 23, v6
	v_add_u32_e32 v7, 0xffffff88, v7
	v_cmp_lt_u32_e32 vcc, 63, v7
	s_nop 1
	v_cndmask_b32_e32 v10, 0, v145, vcc
	v_add_u32_e32 v7, v10, v7
	v_cmp_lt_u32_e64 s[6:7], 31, v7
	s_nop 1
	v_cndmask_b32_e64 v10, 0, v146, s[6:7]
	v_add_u32_e32 v7, v10, v7
	v_cmp_lt_u32_e64 s[8:9], 31, v7
	s_nop 1
	v_cndmask_b32_e64 v10, 0, v146, s[8:9]
	v_add_u32_e32 v7, v10, v7
	v_and_b32_e32 v10, 0x7fffff, v6
	v_or_b32_e32 v16, 0x800000, v10
	v_mad_u64_u32 v[10:11], s[10:11], v16, s38, 0
	v_mov_b32_e32 v62, v11
	v_mad_u64_u32 v[12:13], s[10:11], v16, s39, v[62:63]
	v_mov_b32_e32 v62, v13
	v_mad_u64_u32 v[14:15], s[10:11], v16, s40, v[62:63]
	v_mov_b32_e32 v62, v15
	v_mad_u64_u32 v[18:19], s[10:11], v16, s41, v[62:63]
	v_mov_b32_e32 v62, v19
	v_mad_u64_u32 v[20:21], s[10:11], v16, s42, v[62:63]
	v_mov_b32_e32 v62, v21
	v_mad_u64_u32 v[22:23], s[10:11], v16, s43, v[62:63]
	v_mov_b32_e32 v62, v23
	v_mad_u64_u32 v[24:25], s[10:11], v16, s44, v[62:63]
	v_cndmask_b32_e32 v11, v22, v18, vcc
	v_cndmask_b32_e32 v13, v24, v20, vcc
	v_cndmask_b32_e32 v16, v25, v22, vcc
	v_cndmask_b32_e64 v15, v13, v11, s[6:7]
	v_cndmask_b32_e64 v13, v16, v13, s[6:7]
	v_cndmask_b32_e32 v16, v20, v14, vcc
	v_cndmask_b32_e64 v11, v11, v16, s[6:7]
	v_sub_u32_e32 v19, 32, v7
	v_cmp_eq_u32_e64 s[10:11], 0, v7
	v_cndmask_b32_e32 v7, v18, v12, vcc
	v_cndmask_b32_e64 v13, v13, v15, s[8:9]
	v_cndmask_b32_e64 v15, v15, v11, s[8:9]
	v_cndmask_b32_e64 v12, v16, v7, s[6:7]
	v_alignbit_b32 v20, v13, v15, v19
	v_cndmask_b32_e64 v11, v11, v12, s[8:9]
	v_cndmask_b32_e64 v13, v20, v13, s[10:11]
	v_alignbit_b32 v16, v15, v11, v19
	v_cndmask_b32_e32 v10, v14, v10, vcc
	v_cndmask_b32_e64 v15, v16, v15, s[10:11]
	v_bfe_u32 v20, v13, 29, 1
	v_cndmask_b32_e64 v7, v7, v10, s[6:7]
	v_alignbit_b32 v16, v13, v15, 30
	v_sub_u32_e32 v21, 0, v20
	v_cndmask_b32_e64 v7, v12, v7, s[8:9]
	v_xor_b32_e32 v16, v16, v21
	v_alignbit_b32 v10, v11, v7, v19
	v_cndmask_b32_e64 v10, v10, v11, s[10:11]
	v_ffbh_u32_e32 v12, v16
	v_alignbit_b32 v11, v15, v10, 30
	v_min_u32_e32 v12, 32, v12
	v_alignbit_b32 v7, v10, v7, 30
	v_xor_b32_e32 v11, v11, v21
	v_sub_u32_e32 v14, 31, v12
	v_xor_b32_e32 v7, v7, v21
	v_alignbit_b32 v15, v16, v11, v14
	v_alignbit_b32 v7, v11, v7, v14
	v_alignbit_b32 v10, v15, v7, 9
	v_ffbh_u32_e32 v11, v10
	v_min_u32_e32 v11, 32, v11
	v_lshrrev_b32_e32 v18, 29, v13
	v_not_b32_e32 v14, v11
	v_alignbit_b32 v7, v10, v7, v14
	v_lshlrev_b32_e32 v10, 31, v18
	v_or_b32_e32 v14, 0x33000000, v10
	v_add_lshl_u32 v11, v11, v12, 23
	v_lshrrev_b32_e32 v7, 9, v7
	v_sub_u32_e32 v11, v14, v11
	v_or_b32_e32 v10, 0.5, v10
	v_lshlrev_b32_e32 v12, 23, v12
	v_or_b32_e32 v7, v11, v7
	v_lshrrev_b32_e32 v11, 9, v15
	v_sub_u32_e32 v10, v10, v12
	v_or_b32_e32 v10, v11, v10
	v_mul_f32_e32 v11, 0x3fc90fda, v10
	v_fma_f32 v12, v10, s45, -v11
	v_fmac_f32_e32 v12, 0x33a22168, v10
	v_fmac_f32_e32 v12, 0x3fc90fda, v7
	v_lshrrev_b32_e32 v10, 30, v13
	v_add_f32_e32 v7, v11, v12
	v_add_u32_e32 v10, v20, v10
.LBB0_402:
	s_andn2_saveexec_b64 s[6:7], s[12:13]
	v_mul_f32_e64 v7, |v1|, s46
	v_rndne_f32_e32 v11, v7
	v_cvt_i32_f32_e32 v10, v11
	v_fma_f32 v7, v11, s47, |v1|
	v_fmac_f32_e32 v7, 0xb3a22168, v11
	v_fmac_f32_e32 v7, 0xa7c234c4, v11
	s_or_b64 exec, exec, s[6:7]
	v_mov_b32_e32 v11, v230
	v_mul_f32_e32 v12, v7, v7
	v_and_b32_e32 v13, 1, v10
	v_lshlrev_b32_e32 v10, 30, v10
	v_fmamk_f32 v14, v12, 0xb94c1982, v125
	v_fmamk_f32 v15, v12, 0x37d75334, v143
	v_xor_b32_e32 v6, v6, v1
	v_and_b32_e32 v10, 0x80000000, v10
	v_fmaak_f32 v14, v12, v14, 0xbe2aaa9d
	v_fmaak_f32 v15, v12, v15, 0x3d2aabf7
	v_xor_b32_e32 v6, v6, v10
	v_mul_f32_e32 v10, v12, v14
	v_fmaak_f32 v14, v12, v15, 0xbf000004
	v_fmac_f32_e32 v7, v7, v10
	v_fma_f32 v10, v12, v14, 1.0
	v_cmp_eq_u32_e32 vcc, 0, v13
	s_nop 1
	v_cndmask_b32_e32 v7, v10, v7, vcc
	v_xor_b32_e32 v6, v6, v7
	v_cmp_class_f32_e64 vcc, v1, s49
	s_nop 1
	v_cndmask_b32_e32 v1, v147, v6, vcc
	ds_write_b32 v133, v1 offset:9220
	s_waitcnt vmcnt(0)
	v_mul_f32_e32 v1, v8, v11
	v_and_b32_e32 v6, 0x7fffffff, v1
	v_cmp_nlt_f32_e64 s[6:7], |v1|, s37
	s_and_saveexec_b64 s[8:9], s[6:7]
	s_xor_b64 s[12:13], exec, s[8:9]
	s_cbranch_execz .LBB0_406
	v_lshrrev_b32_e32 v7, 23, v6
	v_add_u32_e32 v7, 0xffffff88, v7
	v_cmp_lt_u32_e32 vcc, 63, v7
	s_nop 1
	v_cndmask_b32_e32 v8, 0, v145, vcc
	v_add_u32_e32 v7, v8, v7
	v_cmp_lt_u32_e64 s[6:7], 31, v7
	s_nop 1
	v_cndmask_b32_e64 v8, 0, v146, s[6:7]
	v_add_u32_e32 v7, v8, v7
	v_cmp_lt_u32_e64 s[8:9], 31, v7
	s_nop 1
	v_cndmask_b32_e64 v8, 0, v146, s[8:9]
	v_add_u32_e32 v7, v8, v7
	v_and_b32_e32 v8, 0x7fffff, v6
	v_or_b32_e32 v8, 0x800000, v8
	v_mad_u64_u32 v[10:11], s[10:11], v8, s38, 0
	v_mov_b32_e32 v62, v11
	v_mad_u64_u32 v[12:13], s[10:11], v8, s39, v[62:63]
	v_mov_b32_e32 v62, v13
	v_mad_u64_u32 v[14:15], s[10:11], v8, s40, v[62:63]
	v_mov_b32_e32 v62, v15
	v_mad_u64_u32 v[18:19], s[10:11], v8, s41, v[62:63]
	v_mov_b32_e32 v62, v19
	v_mad_u64_u32 v[20:21], s[10:11], v8, s42, v[62:63]
	v_mov_b32_e32 v62, v21
	v_mad_u64_u32 v[22:23], s[10:11], v8, s43, v[62:63]
	v_mov_b32_e32 v62, v23
	v_mad_u64_u32 v[24:25], s[10:11], v8, s44, v[62:63]
	v_cndmask_b32_e32 v11, v22, v18, vcc
	v_cndmask_b32_e32 v8, v24, v20, vcc
	v_cndmask_b32_e32 v15, v25, v22, vcc
	v_cndmask_b32_e64 v13, v8, v11, s[6:7]
	v_cndmask_b32_e64 v8, v15, v8, s[6:7]
	v_cndmask_b32_e32 v15, v20, v14, vcc
	v_cndmask_b32_e64 v11, v11, v15, s[6:7]
	v_sub_u32_e32 v16, 32, v7
	v_cmp_eq_u32_e64 s[10:11], 0, v7
	v_cndmask_b32_e32 v7, v18, v12, vcc
	v_cndmask_b32_e64 v8, v8, v13, s[8:9]
	v_cndmask_b32_e64 v13, v13, v11, s[8:9]
	v_cndmask_b32_e64 v12, v15, v7, s[6:7]
	v_alignbit_b32 v19, v8, v13, v16
	v_cndmask_b32_e64 v11, v11, v12, s[8:9]
	v_cndmask_b32_e64 v8, v19, v8, s[10:11]
	v_alignbit_b32 v15, v13, v11, v16
	v_cndmask_b32_e32 v10, v14, v10, vcc
	v_cndmask_b32_e64 v13, v15, v13, s[10:11]
	v_bfe_u32 v19, v8, 29, 1
	v_cndmask_b32_e64 v7, v7, v10, s[6:7]
	v_alignbit_b32 v15, v8, v13, 30
	v_sub_u32_e32 v20, 0, v19
	v_cndmask_b32_e64 v7, v12, v7, s[8:9]
	v_xor_b32_e32 v15, v15, v20
	v_alignbit_b32 v10, v11, v7, v16
	v_cndmask_b32_e64 v10, v10, v11, s[10:11]
	v_ffbh_u32_e32 v12, v15
	v_alignbit_b32 v11, v13, v10, 30
	v_min_u32_e32 v12, 32, v12
	v_alignbit_b32 v7, v10, v7, 30
	v_xor_b32_e32 v11, v11, v20
	v_sub_u32_e32 v13, 31, v12
	v_xor_b32_e32 v7, v7, v20
	v_alignbit_b32 v14, v15, v11, v13
	v_alignbit_b32 v7, v11, v7, v13
	v_alignbit_b32 v10, v14, v7, 9
	v_ffbh_u32_e32 v11, v10
	v_min_u32_e32 v11, 32, v11
	v_lshrrev_b32_e32 v18, 29, v8
	v_not_b32_e32 v13, v11
	v_alignbit_b32 v7, v10, v7, v13
	v_lshlrev_b32_e32 v10, 31, v18
	v_or_b32_e32 v13, 0x33000000, v10
	v_add_lshl_u32 v11, v11, v12, 23
	v_lshrrev_b32_e32 v7, 9, v7
	v_sub_u32_e32 v11, v13, v11
	v_or_b32_e32 v10, 0.5, v10
	v_lshlrev_b32_e32 v12, 23, v12
	v_or_b32_e32 v7, v11, v7
	v_lshrrev_b32_e32 v11, 9, v14
	v_sub_u32_e32 v10, v10, v12
	v_or_b32_e32 v10, v11, v10
	v_mul_f32_e32 v11, 0x3fc90fda, v10
	v_fma_f32 v12, v10, s45, -v11
	v_fmac_f32_e32 v12, 0x33a22168, v10
	v_fmac_f32_e32 v12, 0x3fc90fda, v7
	v_lshrrev_b32_e32 v8, 30, v8
	v_add_f32_e32 v7, v11, v12
	v_add_u32_e32 v8, v19, v8
.LBB0_406:
	s_andn2_saveexec_b64 s[6:7], s[12:13]
	v_mul_f32_e64 v7, |v1|, s46
	v_rndne_f32_e32 v10, v7
	v_cvt_i32_f32_e32 v8, v10
	v_fma_f32 v7, v10, s47, |v1|
	v_fmac_f32_e32 v7, 0xb3a22168, v10
	v_fmac_f32_e32 v7, 0xa7c234c4, v10
	s_or_b64 exec, exec, s[6:7]
	v_mov_b32_e32 v10, v231
	v_mul_f32_e32 v11, v7, v7
	v_and_b32_e32 v12, 1, v8
	v_lshlrev_b32_e32 v8, 30, v8
	v_fmamk_f32 v13, v11, 0xb94c1982, v125
	v_fmamk_f32 v14, v11, 0x37d75334, v143
	v_xor_b32_e32 v6, v6, v1
	v_and_b32_e32 v8, 0x80000000, v8
	v_fmaak_f32 v13, v11, v13, 0xbe2aaa9d
	v_fmaak_f32 v14, v11, v14, 0x3d2aabf7
	v_xor_b32_e32 v6, v6, v8
	v_mul_f32_e32 v8, v11, v13
	v_fmaak_f32 v13, v11, v14, 0xbf000004
	v_fmac_f32_e32 v7, v7, v8
	v_fma_f32 v8, v11, v13, 1.0
	v_cmp_eq_u32_e32 vcc, 0, v12
	s_nop 1
	v_cndmask_b32_e32 v7, v8, v7, vcc
	v_xor_b32_e32 v6, v6, v7
	v_cmp_class_f32_e64 vcc, v1, s49
	s_nop 1
	v_cndmask_b32_e32 v1, v147, v6, vcc
	ds_write_b32 v133, v1 offset:9224
	s_waitcnt vmcnt(0)
	v_mul_f32_e32 v1, v9, v10
	v_and_b32_e32 v6, 0x7fffffff, v1
	v_cmp_nlt_f32_e64 s[6:7], |v1|, s37
	s_and_saveexec_b64 s[8:9], s[6:7]
	s_xor_b64 s[12:13], exec, s[8:9]
	s_cbranch_execz .LBB0_410
	v_lshrrev_b32_e32 v7, 23, v6
	v_add_u32_e32 v7, 0xffffff88, v7
	v_cmp_lt_u32_e32 vcc, 63, v7
	s_nop 1
	v_cndmask_b32_e32 v8, 0, v145, vcc
	v_add_u32_e32 v7, v8, v7
	v_cmp_lt_u32_e64 s[6:7], 31, v7
	s_nop 1
	v_cndmask_b32_e64 v8, 0, v146, s[6:7]
	v_add_u32_e32 v7, v8, v7
	v_cmp_lt_u32_e64 s[8:9], 31, v7
	s_nop 1
	v_cndmask_b32_e64 v8, 0, v146, s[8:9]
	v_add_u32_e32 v7, v8, v7
	v_and_b32_e32 v8, 0x7fffff, v6
	v_or_b32_e32 v16, 0x800000, v8
	v_mad_u64_u32 v[8:9], s[10:11], v16, s38, 0
	v_mov_b32_e32 v62, v9
	v_mad_u64_u32 v[10:11], s[10:11], v16, s39, v[62:63]
	v_mov_b32_e32 v62, v11
	v_mad_u64_u32 v[12:13], s[10:11], v16, s40, v[62:63]
	v_mov_b32_e32 v62, v13
	v_mad_u64_u32 v[14:15], s[10:11], v16, s41, v[62:63]
	v_mov_b32_e32 v62, v15
	v_mad_u64_u32 v[18:19], s[10:11], v16, s42, v[62:63]
	v_mov_b32_e32 v62, v19
	v_mad_u64_u32 v[20:21], s[10:11], v16, s43, v[62:63]
	v_mov_b32_e32 v62, v21
	v_mad_u64_u32 v[22:23], s[10:11], v16, s44, v[62:63]
	v_cndmask_b32_e32 v9, v20, v14, vcc
	v_cndmask_b32_e32 v11, v22, v18, vcc
	v_cndmask_b32_e32 v15, v23, v20, vcc
	v_cndmask_b32_e64 v13, v11, v9, s[6:7]
	v_cndmask_b32_e64 v11, v15, v11, s[6:7]
	v_cndmask_b32_e32 v15, v18, v12, vcc
	v_cndmask_b32_e64 v9, v9, v15, s[6:7]
	v_sub_u32_e32 v16, 32, v7
	v_cmp_eq_u32_e64 s[10:11], 0, v7
	v_cndmask_b32_e32 v7, v14, v10, vcc
	v_cndmask_b32_e64 v11, v11, v13, s[8:9]
	v_cndmask_b32_e64 v13, v13, v9, s[8:9]
	v_cndmask_b32_e64 v10, v15, v7, s[6:7]
	v_alignbit_b32 v18, v11, v13, v16
	v_cndmask_b32_e64 v9, v9, v10, s[8:9]
	v_cndmask_b32_e64 v11, v18, v11, s[10:11]
	v_alignbit_b32 v14, v13, v9, v16
	v_cndmask_b32_e32 v8, v12, v8, vcc
	v_cndmask_b32_e64 v13, v14, v13, s[10:11]
	v_bfe_u32 v18, v11, 29, 1
	v_cndmask_b32_e64 v7, v7, v8, s[6:7]
	v_alignbit_b32 v14, v11, v13, 30
	v_sub_u32_e32 v19, 0, v18
	v_cndmask_b32_e64 v7, v10, v7, s[8:9]
	v_xor_b32_e32 v14, v14, v19
	v_alignbit_b32 v8, v9, v7, v16
	v_cndmask_b32_e64 v8, v8, v9, s[10:11]
	v_ffbh_u32_e32 v10, v14
	v_alignbit_b32 v9, v13, v8, 30
	v_min_u32_e32 v10, 32, v10
	v_alignbit_b32 v7, v8, v7, 30
	v_xor_b32_e32 v9, v9, v19
	v_sub_u32_e32 v12, 31, v10
	v_xor_b32_e32 v7, v7, v19
	v_alignbit_b32 v13, v14, v9, v12
	v_alignbit_b32 v7, v9, v7, v12
	v_alignbit_b32 v8, v13, v7, 9
	v_ffbh_u32_e32 v9, v8
	v_min_u32_e32 v9, 32, v9
	v_lshrrev_b32_e32 v15, 29, v11
	v_not_b32_e32 v12, v9
	v_alignbit_b32 v7, v8, v7, v12
	v_lshlrev_b32_e32 v8, 31, v15
	v_or_b32_e32 v12, 0x33000000, v8
	v_add_lshl_u32 v9, v9, v10, 23
	v_lshrrev_b32_e32 v7, 9, v7
	v_sub_u32_e32 v9, v12, v9
	v_or_b32_e32 v8, 0.5, v8
	v_lshlrev_b32_e32 v10, 23, v10
	v_or_b32_e32 v7, v9, v7
	v_lshrrev_b32_e32 v9, 9, v13
	v_sub_u32_e32 v8, v8, v10
	v_or_b32_e32 v8, v9, v8
	v_mul_f32_e32 v9, 0x3fc90fda, v8
	v_fma_f32 v10, v8, s45, -v9
	v_fmac_f32_e32 v10, 0x33a22168, v8
	v_fmac_f32_e32 v10, 0x3fc90fda, v7
	v_lshrrev_b32_e32 v8, 30, v11
	v_add_f32_e32 v7, v9, v10
	v_add_u32_e32 v8, v18, v8
.LBB0_410:
	s_andn2_saveexec_b64 s[6:7], s[12:13]
	v_mul_f32_e64 v7, |v1|, s46
	v_rndne_f32_e32 v9, v7
	v_cvt_i32_f32_e32 v8, v9
	v_fma_f32 v7, v9, s47, |v1|
	v_fmac_f32_e32 v7, 0xb3a22168, v9
	v_fmac_f32_e32 v7, 0xa7c234c4, v9
	s_or_b64 exec, exec, s[6:7]
	v_mov_b32_e32 v9, v232
	v_mul_f32_e32 v10, v7, v7
	v_and_b32_e32 v11, 1, v8
	v_lshlrev_b32_e32 v8, 30, v8
	v_fmamk_f32 v12, v10, 0xb94c1982, v125
	v_fmamk_f32 v13, v10, 0x37d75334, v143
	v_xor_b32_e32 v6, v6, v1
	v_and_b32_e32 v8, 0x80000000, v8
	v_fmaak_f32 v12, v10, v12, 0xbe2aaa9d
	v_fmaak_f32 v13, v10, v13, 0x3d2aabf7
	v_xor_b32_e32 v6, v6, v8
	v_mul_f32_e32 v8, v10, v12
	v_fmaak_f32 v12, v10, v13, 0xbf000004
	v_fmac_f32_e32 v7, v7, v8
	v_fma_f32 v8, v10, v12, 1.0
	v_cmp_eq_u32_e32 vcc, 0, v11
	s_nop 1
	v_cndmask_b32_e32 v7, v8, v7, vcc
	v_xor_b32_e32 v6, v6, v7
	v_cmp_class_f32_e64 vcc, v1, s49
	s_nop 1
	v_cndmask_b32_e32 v1, v147, v6, vcc
	ds_write_b32 v133, v1 offset:9228
	s_waitcnt vmcnt(0)
	v_mul_f32_e32 v1, v2, v9
	v_and_b32_e32 v2, 0x7fffffff, v1
	v_cmp_nlt_f32_e64 s[6:7], |v1|, s37
	s_and_saveexec_b64 s[8:9], s[6:7]
	s_xor_b64 s[12:13], exec, s[8:9]
	s_cbranch_execz .LBB0_414
	v_lshrrev_b32_e32 v6, 23, v2
	v_add_u32_e32 v6, 0xffffff88, v6
	v_cmp_lt_u32_e32 vcc, 63, v6
	s_nop 1
	v_cndmask_b32_e32 v7, 0, v145, vcc
	v_add_u32_e32 v6, v7, v6
	v_cmp_lt_u32_e64 s[6:7], 31, v6
	s_nop 1
	v_cndmask_b32_e64 v7, 0, v146, s[6:7]
	v_add_u32_e32 v6, v7, v6
	v_cmp_lt_u32_e64 s[8:9], 31, v6
	s_nop 1
	v_cndmask_b32_e64 v7, 0, v146, s[8:9]
	v_add_u32_e32 v16, v7, v6
	v_and_b32_e32 v6, 0x7fffff, v2
	v_or_b32_e32 v20, 0x800000, v6
	v_mad_u64_u32 v[6:7], s[10:11], v20, s38, 0
	v_mov_b32_e32 v62, v7
	v_mad_u64_u32 v[8:9], s[10:11], v20, s39, v[62:63]
	v_mov_b32_e32 v62, v9
	v_mad_u64_u32 v[10:11], s[10:11], v20, s40, v[62:63]
	v_mov_b32_e32 v62, v11
	v_mad_u64_u32 v[12:13], s[10:11], v20, s41, v[62:63]
	v_mov_b32_e32 v62, v13
	v_mad_u64_u32 v[14:15], s[10:11], v20, s42, v[62:63]
	v_mov_b32_e32 v62, v15
	v_mad_u64_u32 v[18:19], s[10:11], v20, s43, v[62:63]
	v_mov_b32_e32 v62, v19
	v_mad_u64_u32 v[20:21], s[10:11], v20, s44, v[62:63]
	v_cndmask_b32_e32 v7, v18, v12, vcc
	v_cndmask_b32_e32 v9, v20, v14, vcc
	v_cndmask_b32_e32 v13, v21, v18, vcc
	v_cndmask_b32_e64 v11, v9, v7, s[6:7]
	v_cndmask_b32_e64 v9, v13, v9, s[6:7]
	v_cndmask_b32_e32 v13, v14, v10, vcc
	v_cndmask_b32_e64 v7, v7, v13, s[6:7]
	v_cndmask_b32_e32 v8, v12, v8, vcc
	v_cndmask_b32_e64 v9, v9, v11, s[8:9]
	v_cndmask_b32_e64 v11, v11, v7, s[8:9]
	v_sub_u32_e32 v14, 32, v16
	v_cndmask_b32_e64 v12, v13, v8, s[6:7]
	v_alignbit_b32 v15, v9, v11, v14
	v_cmp_eq_u32_e64 s[10:11], 0, v16
	v_cndmask_b32_e64 v7, v7, v12, s[8:9]
	v_alignbit_b32 v13, v11, v7, v14
	v_cndmask_b32_e64 v9, v15, v9, s[10:11]
	v_cndmask_b32_e32 v6, v10, v6, vcc
	v_cndmask_b32_e64 v11, v13, v11, s[10:11]
	v_bfe_u32 v16, v9, 29, 1
	v_cndmask_b32_e64 v6, v8, v6, s[6:7]
	v_alignbit_b32 v13, v9, v11, 30
	v_sub_u32_e32 v18, 0, v16
	v_cndmask_b32_e64 v6, v12, v6, s[8:9]
	v_xor_b32_e32 v13, v13, v18
	v_alignbit_b32 v8, v7, v6, v14
	v_cndmask_b32_e64 v7, v8, v7, s[10:11]
	v_ffbh_u32_e32 v10, v13
	v_alignbit_b32 v8, v11, v7, 30
	v_min_u32_e32 v10, 32, v10
	v_alignbit_b32 v6, v7, v6, 30
	v_xor_b32_e32 v8, v8, v18
	v_sub_u32_e32 v11, 31, v10
	v_xor_b32_e32 v6, v6, v18
	v_alignbit_b32 v12, v13, v8, v11
	v_alignbit_b32 v6, v8, v6, v11
	v_alignbit_b32 v7, v12, v6, 9
	v_ffbh_u32_e32 v8, v7
	v_min_u32_e32 v8, 32, v8
	v_lshrrev_b32_e32 v15, 29, v9
	v_not_b32_e32 v11, v8
	v_alignbit_b32 v6, v7, v6, v11
	v_lshlrev_b32_e32 v7, 31, v15
	v_or_b32_e32 v11, 0x33000000, v7
	v_add_lshl_u32 v8, v8, v10, 23
	v_lshrrev_b32_e32 v6, 9, v6
	v_sub_u32_e32 v8, v11, v8
	v_or_b32_e32 v7, 0.5, v7
	v_lshlrev_b32_e32 v10, 23, v10
	v_or_b32_e32 v6, v8, v6
	v_lshrrev_b32_e32 v8, 9, v12
	v_sub_u32_e32 v7, v7, v10
	v_or_b32_e32 v7, v8, v7
	v_mul_f32_e32 v8, 0x3fc90fda, v7
	v_fma_f32 v10, v7, s45, -v8
	v_fmac_f32_e32 v10, 0x33a22168, v7
	v_fmac_f32_e32 v10, 0x3fc90fda, v6
	v_lshrrev_b32_e32 v7, 30, v9
	v_add_f32_e32 v6, v8, v10
	v_add_u32_e32 v7, v16, v7
.LBB0_414:
	s_andn2_saveexec_b64 s[6:7], s[12:13]
	v_mul_f32_e64 v6, |v1|, s46
	v_rndne_f32_e32 v8, v6
	v_cvt_i32_f32_e32 v7, v8
	v_fma_f32 v6, v8, s47, |v1|
	v_fmac_f32_e32 v6, 0xb3a22168, v8
	v_fmac_f32_e32 v6, 0xa7c234c4, v8
	s_or_b64 exec, exec, s[6:7]
	v_mov_b32_e32 v8, v233
	v_mul_f32_e32 v9, v6, v6
	v_and_b32_e32 v10, 1, v7
	v_lshlrev_b32_e32 v7, 30, v7
	v_fmamk_f32 v11, v9, 0xb94c1982, v125
	v_fmamk_f32 v12, v9, 0x37d75334, v143
	v_xor_b32_e32 v2, v2, v1
	v_and_b32_e32 v7, 0x80000000, v7
	v_fmaak_f32 v11, v9, v11, 0xbe2aaa9d
	v_fmaak_f32 v12, v9, v12, 0x3d2aabf7
	v_xor_b32_e32 v2, v2, v7
	v_mul_f32_e32 v7, v9, v11
	v_fmaak_f32 v11, v9, v12, 0xbf000004
	v_fmac_f32_e32 v6, v6, v7
	v_fma_f32 v7, v9, v11, 1.0
	v_cmp_eq_u32_e32 vcc, 0, v10
	s_nop 1
	v_cndmask_b32_e32 v6, v7, v6, vcc
	v_xor_b32_e32 v2, v2, v6
	v_cmp_class_f32_e64 vcc, v1, s49
	s_nop 1
	v_cndmask_b32_e32 v1, v147, v2, vcc
	ds_write_b32 v133, v1 offset:9232
	s_waitcnt vmcnt(0)
	v_mul_f32_e32 v1, v3, v8
	v_and_b32_e32 v2, 0x7fffffff, v1
	v_cmp_nlt_f32_e64 s[6:7], |v1|, s37
	s_and_saveexec_b64 s[8:9], s[6:7]
	s_xor_b64 s[12:13], exec, s[8:9]
	s_cbranch_execz .LBB0_418
	v_lshrrev_b32_e32 v3, 23, v2
	v_add_u32_e32 v3, 0xffffff88, v3
	v_cmp_lt_u32_e32 vcc, 63, v3
	s_nop 1
	v_cndmask_b32_e32 v6, 0, v145, vcc
	v_add_u32_e32 v3, v6, v3
	v_cmp_lt_u32_e64 s[6:7], 31, v3
	s_nop 1
	v_cndmask_b32_e64 v6, 0, v146, s[6:7]
	v_add_u32_e32 v3, v6, v3
	v_cmp_lt_u32_e64 s[8:9], 31, v3
	s_nop 1
	v_cndmask_b32_e64 v6, 0, v146, s[8:9]
	v_add_u32_e32 v3, v6, v3
	v_and_b32_e32 v6, 0x7fffff, v2
	v_or_b32_e32 v16, 0x800000, v6
	v_mad_u64_u32 v[6:7], s[10:11], v16, s38, 0
	v_mov_b32_e32 v62, v7
	v_mad_u64_u32 v[8:9], s[10:11], v16, s39, v[62:63]
	v_mov_b32_e32 v62, v9
	v_mad_u64_u32 v[10:11], s[10:11], v16, s40, v[62:63]
	v_mov_b32_e32 v62, v11
	v_mad_u64_u32 v[12:13], s[10:11], v16, s41, v[62:63]
	v_mov_b32_e32 v62, v13
	v_mad_u64_u32 v[14:15], s[10:11], v16, s42, v[62:63]
	v_mov_b32_e32 v62, v15
	v_mad_u64_u32 v[18:19], s[10:11], v16, s43, v[62:63]
	v_mov_b32_e32 v62, v19
	v_mad_u64_u32 v[20:21], s[10:11], v16, s44, v[62:63]
	v_cndmask_b32_e32 v7, v18, v12, vcc
	v_cndmask_b32_e32 v9, v20, v14, vcc
	v_cndmask_b32_e32 v13, v21, v18, vcc
	v_cndmask_b32_e64 v11, v9, v7, s[6:7]
	v_cndmask_b32_e64 v9, v13, v9, s[6:7]
	v_cndmask_b32_e32 v13, v14, v10, vcc
	v_cndmask_b32_e64 v7, v7, v13, s[6:7]
	v_sub_u32_e32 v14, 32, v3
	v_cmp_eq_u32_e64 s[10:11], 0, v3
	v_cndmask_b32_e32 v3, v12, v8, vcc
	v_cndmask_b32_e64 v9, v9, v11, s[8:9]
	v_cndmask_b32_e64 v11, v11, v7, s[8:9]
	v_cndmask_b32_e64 v8, v13, v3, s[6:7]
	v_alignbit_b32 v15, v9, v11, v14
	v_cndmask_b32_e64 v7, v7, v8, s[8:9]
	v_cndmask_b32_e64 v9, v15, v9, s[10:11]
	v_alignbit_b32 v12, v11, v7, v14
	v_cndmask_b32_e32 v6, v10, v6, vcc
	v_cndmask_b32_e64 v11, v12, v11, s[10:11]
	v_bfe_u32 v15, v9, 29, 1
	v_cndmask_b32_e64 v3, v3, v6, s[6:7]
	v_alignbit_b32 v12, v9, v11, 30
	v_sub_u32_e32 v16, 0, v15
	v_cndmask_b32_e64 v3, v8, v3, s[8:9]
	v_xor_b32_e32 v12, v12, v16
	v_alignbit_b32 v6, v7, v3, v14
	v_cndmask_b32_e64 v6, v6, v7, s[10:11]
	v_ffbh_u32_e32 v8, v12
	v_alignbit_b32 v7, v11, v6, 30
	v_min_u32_e32 v8, 32, v8
	v_alignbit_b32 v3, v6, v3, 30
	v_xor_b32_e32 v7, v7, v16
	v_sub_u32_e32 v10, 31, v8
	v_xor_b32_e32 v3, v3, v16
	v_alignbit_b32 v11, v12, v7, v10
	v_alignbit_b32 v3, v7, v3, v10
	v_alignbit_b32 v6, v11, v3, 9
	v_ffbh_u32_e32 v7, v6
	v_min_u32_e32 v7, 32, v7
	v_lshrrev_b32_e32 v13, 29, v9
	v_not_b32_e32 v10, v7
	v_alignbit_b32 v3, v6, v3, v10
	v_lshlrev_b32_e32 v6, 31, v13
	v_or_b32_e32 v10, 0x33000000, v6
	v_add_lshl_u32 v7, v7, v8, 23
	v_lshrrev_b32_e32 v3, 9, v3
	v_sub_u32_e32 v7, v10, v7
	v_or_b32_e32 v6, 0.5, v6
	v_lshlrev_b32_e32 v8, 23, v8
	v_or_b32_e32 v3, v7, v3
	v_lshrrev_b32_e32 v7, 9, v11
	v_sub_u32_e32 v6, v6, v8
	v_or_b32_e32 v6, v7, v6
	v_mul_f32_e32 v7, 0x3fc90fda, v6
	v_fma_f32 v8, v6, s45, -v7
	v_fmac_f32_e32 v8, 0x33a22168, v6
	v_fmac_f32_e32 v8, 0x3fc90fda, v3
	v_lshrrev_b32_e32 v6, 30, v9
	v_add_f32_e32 v3, v7, v8
	v_add_u32_e32 v6, v15, v6
.LBB0_418:
	s_andn2_saveexec_b64 s[6:7], s[12:13]
	v_mul_f32_e64 v3, |v1|, s46
	v_rndne_f32_e32 v7, v3
	v_cvt_i32_f32_e32 v6, v7
	v_fma_f32 v3, v7, s47, |v1|
	v_fmac_f32_e32 v3, 0xb3a22168, v7
	v_fmac_f32_e32 v3, 0xa7c234c4, v7
	s_or_b64 exec, exec, s[6:7]
	v_mov_b32_e32 v7, v234
	v_mul_f32_e32 v8, v3, v3
	v_and_b32_e32 v9, 1, v6
	v_lshlrev_b32_e32 v6, 30, v6
	v_fmamk_f32 v10, v8, 0xb94c1982, v125
	v_fmamk_f32 v11, v8, 0x37d75334, v143
	v_xor_b32_e32 v2, v2, v1
	v_and_b32_e32 v6, 0x80000000, v6
	v_fmaak_f32 v10, v8, v10, 0xbe2aaa9d
	v_fmaak_f32 v11, v8, v11, 0x3d2aabf7
	v_xor_b32_e32 v2, v2, v6
	v_mul_f32_e32 v6, v8, v10
	v_fmaak_f32 v10, v8, v11, 0xbf000004
	v_fmac_f32_e32 v3, v3, v6
	v_fma_f32 v6, v8, v10, 1.0
	v_cmp_eq_u32_e32 vcc, 0, v9
	s_nop 1
	v_cndmask_b32_e32 v3, v6, v3, vcc
	v_xor_b32_e32 v2, v2, v3
	v_cmp_class_f32_e64 vcc, v1, s49
	s_nop 1
	v_cndmask_b32_e32 v1, v147, v2, vcc
	ds_write_b32 v133, v1 offset:9236
	s_waitcnt vmcnt(0)
	v_mul_f32_e32 v1, v4, v7
	v_and_b32_e32 v2, 0x7fffffff, v1
	v_cmp_nlt_f32_e64 s[6:7], |v1|, s37
	s_and_saveexec_b64 s[8:9], s[6:7]
	s_xor_b64 s[12:13], exec, s[8:9]
	s_cbranch_execz .LBB0_422
	v_lshrrev_b32_e32 v3, 23, v2
	v_add_u32_e32 v3, 0xffffff88, v3
	v_cmp_lt_u32_e32 vcc, 63, v3
	s_nop 1
	v_cndmask_b32_e32 v4, 0, v145, vcc
	v_add_u32_e32 v3, v4, v3
	v_cmp_lt_u32_e64 s[6:7], 31, v3
	s_nop 1
	v_cndmask_b32_e64 v4, 0, v146, s[6:7]
	v_add_u32_e32 v3, v4, v3
	v_cmp_lt_u32_e64 s[8:9], 31, v3
	s_nop 1
	v_cndmask_b32_e64 v4, 0, v146, s[8:9]
	v_add_u32_e32 v3, v4, v3
	v_and_b32_e32 v4, 0x7fffff, v2
	v_or_b32_e32 v4, 0x800000, v4
	v_mad_u64_u32 v[6:7], s[10:11], v4, s38, 0
	v_mov_b32_e32 v62, v7
	v_mad_u64_u32 v[8:9], s[10:11], v4, s39, v[62:63]
	v_mov_b32_e32 v62, v9
	v_mad_u64_u32 v[10:11], s[10:11], v4, s40, v[62:63]
	v_mov_b32_e32 v62, v11
	v_mad_u64_u32 v[12:13], s[10:11], v4, s41, v[62:63]
	v_mov_b32_e32 v62, v13
	v_mad_u64_u32 v[14:15], s[10:11], v4, s42, v[62:63]
	v_mov_b32_e32 v62, v15
	v_mad_u64_u32 v[18:19], s[10:11], v4, s43, v[62:63]
	v_mov_b32_e32 v62, v19
	v_mad_u64_u32 v[20:21], s[10:11], v4, s44, v[62:63]
	v_cndmask_b32_e32 v7, v18, v12, vcc
	v_cndmask_b32_e32 v4, v20, v14, vcc
	v_cndmask_b32_e32 v11, v21, v18, vcc
	v_cndmask_b32_e64 v9, v4, v7, s[6:7]
	v_cndmask_b32_e64 v4, v11, v4, s[6:7]
	v_cndmask_b32_e32 v11, v14, v10, vcc
	v_cndmask_b32_e64 v7, v7, v11, s[6:7]
	v_sub_u32_e32 v13, 32, v3
	v_cmp_eq_u32_e64 s[10:11], 0, v3
	v_cndmask_b32_e32 v3, v12, v8, vcc
	v_cndmask_b32_e64 v4, v4, v9, s[8:9]
	v_cndmask_b32_e64 v9, v9, v7, s[8:9]
	v_cndmask_b32_e64 v8, v11, v3, s[6:7]
	v_alignbit_b32 v14, v4, v9, v13
	v_cndmask_b32_e64 v7, v7, v8, s[8:9]
	v_cndmask_b32_e64 v4, v14, v4, s[10:11]
	v_alignbit_b32 v11, v9, v7, v13
	v_cndmask_b32_e32 v6, v10, v6, vcc
	v_cndmask_b32_e64 v9, v11, v9, s[10:11]
	v_bfe_u32 v14, v4, 29, 1
	v_cndmask_b32_e64 v3, v3, v6, s[6:7]
	v_alignbit_b32 v11, v4, v9, 30
	v_sub_u32_e32 v15, 0, v14
	v_cndmask_b32_e64 v3, v8, v3, s[8:9]
	v_xor_b32_e32 v11, v11, v15
	v_alignbit_b32 v6, v7, v3, v13
	v_cndmask_b32_e64 v6, v6, v7, s[10:11]
	v_ffbh_u32_e32 v8, v11
	v_alignbit_b32 v7, v9, v6, 30
	v_min_u32_e32 v8, 32, v8
	v_alignbit_b32 v3, v6, v3, 30
	v_xor_b32_e32 v7, v7, v15
	v_sub_u32_e32 v9, 31, v8
	v_xor_b32_e32 v3, v3, v15
	v_alignbit_b32 v10, v11, v7, v9
	v_alignbit_b32 v3, v7, v3, v9
	v_alignbit_b32 v6, v10, v3, 9
	v_ffbh_u32_e32 v7, v6
	v_min_u32_e32 v7, 32, v7
	v_lshrrev_b32_e32 v12, 29, v4
	v_not_b32_e32 v9, v7
	v_alignbit_b32 v3, v6, v3, v9
	v_lshlrev_b32_e32 v6, 31, v12
	v_or_b32_e32 v9, 0x33000000, v6
	v_add_lshl_u32 v7, v7, v8, 23
	v_lshrrev_b32_e32 v3, 9, v3
	v_sub_u32_e32 v7, v9, v7
	v_or_b32_e32 v6, 0.5, v6
	v_lshlrev_b32_e32 v8, 23, v8
	v_or_b32_e32 v3, v7, v3
	v_lshrrev_b32_e32 v7, 9, v10
	v_sub_u32_e32 v6, v6, v8
	v_or_b32_e32 v6, v7, v6
	v_mul_f32_e32 v7, 0x3fc90fda, v6
	v_fma_f32 v8, v6, s45, -v7
	v_fmac_f32_e32 v8, 0x33a22168, v6
	v_fmac_f32_e32 v8, 0x3fc90fda, v3
	v_lshrrev_b32_e32 v4, 30, v4
	v_add_f32_e32 v3, v7, v8
	v_add_u32_e32 v4, v14, v4
.LBB0_422:
	s_andn2_saveexec_b64 s[6:7], s[12:13]
	v_mul_f32_e64 v3, |v1|, s46
	v_rndne_f32_e32 v6, v3
	v_cvt_i32_f32_e32 v4, v6
	v_fma_f32 v3, v6, s47, |v1|
	v_fmac_f32_e32 v3, 0xb3a22168, v6
	v_fmac_f32_e32 v3, 0xa7c234c4, v6
	s_or_b64 exec, exec, s[6:7]
	v_mov_b32_e32 v6, v235
	v_mul_f32_e32 v7, v3, v3
	v_and_b32_e32 v8, 1, v4
	v_lshlrev_b32_e32 v4, 30, v4
	v_fmamk_f32 v9, v7, 0xb94c1982, v125
	v_fmamk_f32 v10, v7, 0x37d75334, v143
	v_xor_b32_e32 v2, v2, v1
	v_and_b32_e32 v4, 0x80000000, v4
	v_fmaak_f32 v9, v7, v9, 0xbe2aaa9d
	v_fmaak_f32 v10, v7, v10, 0x3d2aabf7
	v_xor_b32_e32 v2, v2, v4
	v_mul_f32_e32 v4, v7, v9
	v_fmaak_f32 v9, v7, v10, 0xbf000004
	v_fmac_f32_e32 v3, v3, v4
	v_fma_f32 v4, v7, v9, 1.0
	v_cmp_eq_u32_e32 vcc, 0, v8
	s_nop 1
	v_cndmask_b32_e32 v3, v4, v3, vcc
	v_xor_b32_e32 v2, v2, v3
	v_cmp_class_f32_e64 vcc, v1, s49
	s_nop 1
	v_cndmask_b32_e32 v1, v147, v2, vcc
	ds_write_b32 v133, v1 offset:9240
	s_waitcnt vmcnt(0)
	v_mul_f32_e32 v1, v5, v6
	v_and_b32_e32 v2, 0x7fffffff, v1
	v_cmp_nlt_f32_e64 s[6:7], |v1|, s37
	s_and_saveexec_b64 s[8:9], s[6:7]
	s_xor_b64 s[12:13], exec, s[8:9]
	s_cbranch_execz .LBB0_426
	v_lshrrev_b32_e32 v3, 23, v2
	v_add_u32_e32 v3, 0xffffff88, v3
	v_cmp_lt_u32_e32 vcc, 63, v3
	s_nop 1
	v_cndmask_b32_e32 v4, 0, v145, vcc
	v_add_u32_e32 v3, v4, v3
	v_cmp_lt_u32_e64 s[6:7], 31, v3
	s_nop 1
	v_cndmask_b32_e64 v4, 0, v146, s[6:7]
	v_add_u32_e32 v3, v4, v3
	v_cmp_lt_u32_e64 s[8:9], 31, v3
	s_nop 1
	v_cndmask_b32_e64 v4, 0, v146, s[8:9]
	v_add_u32_e32 v3, v4, v3
	v_and_b32_e32 v4, 0x7fffff, v2
	v_or_b32_e32 v16, 0x800000, v4
	v_mad_u64_u32 v[4:5], s[10:11], v16, s38, 0
	v_mov_b32_e32 v62, v5
	v_mad_u64_u32 v[6:7], s[10:11], v16, s39, v[62:63]
	v_mov_b32_e32 v62, v7
	v_mad_u64_u32 v[8:9], s[10:11], v16, s40, v[62:63]
	v_mov_b32_e32 v62, v9
	v_mad_u64_u32 v[10:11], s[10:11], v16, s41, v[62:63]
	v_mov_b32_e32 v62, v11
	v_mad_u64_u32 v[12:13], s[10:11], v16, s42, v[62:63]
	v_mov_b32_e32 v62, v13
	v_mad_u64_u32 v[14:15], s[10:11], v16, s43, v[62:63]
	v_mov_b32_e32 v62, v15
	v_mad_u64_u32 v[18:19], s[10:11], v16, s44, v[62:63]
	v_cndmask_b32_e32 v5, v14, v10, vcc
	v_cndmask_b32_e32 v7, v18, v12, vcc
	v_cndmask_b32_e32 v11, v19, v14, vcc
	v_cndmask_b32_e64 v9, v7, v5, s[6:7]
	v_cndmask_b32_e64 v7, v11, v7, s[6:7]
	v_cndmask_b32_e32 v11, v12, v8, vcc
	v_cndmask_b32_e64 v5, v5, v11, s[6:7]
	v_cndmask_b32_e64 v7, v7, v9, s[8:9]
	v_cndmask_b32_e64 v9, v9, v5, s[8:9]
	v_sub_u32_e32 v12, 32, v3
	v_alignbit_b32 v13, v7, v9, v12
	v_cmp_eq_u32_e64 s[10:11], 0, v3
	v_cndmask_b32_e32 v6, v10, v6, vcc
	v_cndmask_b32_e32 v4, v8, v4, vcc
	v_cndmask_b32_e64 v3, v13, v7, s[10:11]
	v_cndmask_b32_e64 v7, v11, v6, s[6:7]
	v_cndmask_b32_e64 v5, v5, v7, s[8:9]
	v_alignbit_b32 v10, v9, v5, v12
	v_cndmask_b32_e64 v9, v10, v9, s[10:11]
	v_bfe_u32 v13, v3, 29, 1
	v_cndmask_b32_e64 v4, v6, v4, s[6:7]
	v_alignbit_b32 v10, v3, v9, 30
	v_sub_u32_e32 v14, 0, v13
	v_cndmask_b32_e64 v4, v7, v4, s[8:9]
	v_xor_b32_e32 v10, v10, v14
	v_alignbit_b32 v6, v5, v4, v12
	v_cndmask_b32_e64 v5, v6, v5, s[10:11]
	v_ffbh_u32_e32 v7, v10
	v_alignbit_b32 v6, v9, v5, 30
	v_min_u32_e32 v7, 32, v7
	v_alignbit_b32 v4, v5, v4, 30
	v_xor_b32_e32 v6, v6, v14
	v_sub_u32_e32 v8, 31, v7
	v_xor_b32_e32 v4, v4, v14
	v_alignbit_b32 v9, v10, v6, v8
	v_alignbit_b32 v4, v6, v4, v8
	v_alignbit_b32 v5, v9, v4, 9
	v_ffbh_u32_e32 v6, v5
	v_min_u32_e32 v6, 32, v6
	v_lshrrev_b32_e32 v11, 29, v3
	v_not_b32_e32 v8, v6
	v_alignbit_b32 v4, v5, v4, v8
	v_lshlrev_b32_e32 v5, 31, v11
	v_or_b32_e32 v8, 0x33000000, v5
	v_add_lshl_u32 v6, v6, v7, 23
	v_lshrrev_b32_e32 v4, 9, v4
	v_sub_u32_e32 v6, v8, v6
	v_or_b32_e32 v5, 0.5, v5
	v_lshlrev_b32_e32 v7, 23, v7
	v_or_b32_e32 v4, v6, v4
	v_lshrrev_b32_e32 v6, 9, v9
	v_sub_u32_e32 v5, v5, v7
	v_or_b32_e32 v5, v6, v5
	v_mul_f32_e32 v6, 0x3fc90fda, v5
	v_fma_f32 v7, v5, s45, -v6
	v_fmac_f32_e32 v7, 0x33a22168, v5
	v_fmac_f32_e32 v7, 0x3fc90fda, v4
	v_lshrrev_b32_e32 v3, 30, v3
	v_add_f32_e32 v4, v6, v7
	v_add_u32_e32 v3, v13, v3
.LBB0_426:
	s_andn2_saveexec_b64 s[6:7], s[12:13]
	v_mul_f32_e64 v3, |v1|, s46
	v_rndne_f32_e32 v5, v3
	v_cvt_i32_f32_e32 v3, v5
	v_fma_f32 v4, v5, s47, |v1|
	v_fmac_f32_e32 v4, 0xb3a22168, v5
	v_fmac_f32_e32 v4, 0xa7c234c4, v5
	s_or_b64 exec, exec, s[6:7]
	v_mul_f32_e32 v5, v4, v4
	v_fmamk_f32 v6, v5, 0xb94c1982, v125
	v_fmaak_f32 v6, v5, v6, 0xbe2aaa9d
	v_mul_f32_e32 v6, v5, v6
	v_fmac_f32_e32 v4, v4, v6
	v_fmamk_f32 v6, v5, 0x37d75334, v143
	v_fmaak_f32 v6, v5, v6, 0x3d2aabf7
	v_fmaak_f32 v6, v5, v6, 0xbf000004
	v_fma_f32 v5, v5, v6, 1.0
	v_and_b32_e32 v6, 1, v3
	v_lshlrev_b32_e32 v3, 30, v3
	v_cmp_eq_u32_e32 vcc, 0, v6
	v_and_b32_e32 v3, 0x80000000, v3
	v_xor_b32_e32 v2, v2, v1
	v_cndmask_b32_e32 v4, v5, v4, vcc
	v_xor_b32_e32 v2, v2, v3
	v_xor_b32_e32 v2, v2, v4
	v_cmp_class_f32_e64 vcc, v1, s49
	s_mov_b32 s6, 0
	s_nop 0
	v_cndmask_b32_e32 v1, v147, v2, vcc
	ds_write_b32 v133, v1 offset:9244
	s_waitcnt lgkmcnt(0)
	s_barrier
	v_mov_b64_e32 v[2:3], v[240:241]
	v_mov_b64_e32 v[4:5], v[242:243]
	v_mov_b64_e32 v[6:7], v[236:237]
	v_mov_b64_e32 v[8:9], v[238:239]
	v_mov_b32_e32 v1, v142
	v_add_u32_e32 v14, s6, v141
	ds_read_b128 v[10:13], v1
	ds_read_b128 v[18:21], v1 offset:16
	ds_read_b32 v14, v14
	s_add_i32 s6, s6, 4
	v_add_u32_e32 v1, 0x100, v1
.LBB0_429:
	v_add_u32_e32 v216, s6, v141
	ds_read_b128 v[208:211], v1
	ds_read_b128 v[212:215], v1 offset:16
	ds_read_b32 v216, v216
	s_add_i32 s6, s6, 4
	v_add_u32_e32 v1, 0x100, v1
	s_waitcnt vmcnt(0) lgkmcnt(3)
	v_pk_fma_f32 v[6:7], v[14:15], v[10:11], v[6:7] op_sel_hi:[0,1,1]
	v_pk_fma_f32 v[8:9], v[14:15], v[12:13], v[8:9] op_sel_hi:[0,1,1]
	v_pk_fma_f32 v[2:3], v[14:15], v[18:19], v[2:3] op_sel_hi:[0,1,1]
	v_pk_fma_f32 v[4:5], v[14:15], v[20:21], v[4:5] op_sel_hi:[0,1,1]
	v_add_u32_e32 v14, s6, v141
	ds_read_b128 v[10:13], v1
	ds_read_b128 v[18:21], v1 offset:16
	ds_read_b32 v14, v14
	s_add_i32 s6, s6, 4
	v_add_u32_e32 v1, 0x100, v1
	s_waitcnt lgkmcnt(3)
	v_pk_fma_f32 v[6:7], v[216:217], v[208:209], v[6:7] op_sel_hi:[0,1,1]
	v_pk_fma_f32 v[8:9], v[216:217], v[210:211], v[8:9] op_sel_hi:[0,1,1]
	v_pk_fma_f32 v[2:3], v[216:217], v[212:213], v[2:3] op_sel_hi:[0,1,1]
	v_pk_fma_f32 v[4:5], v[216:217], v[214:215], v[4:5] op_sel_hi:[0,1,1]
	s_cmpk_eq_i32 s6, 0xfc
	s_cbranch_scc0 .LBB0_429
	v_add_u32_e32 v216, s6, v141
	ds_read_b128 v[208:211], v1
	ds_read_b128 v[212:215], v1 offset:16
	ds_read_b32 v216, v216
	s_add_i32 s6, s6, 4
	v_add_u32_e32 v1, 0x100, v1
	s_waitcnt lgkmcnt(3)
	v_pk_fma_f32 v[6:7], v[14:15], v[10:11], v[6:7] op_sel_hi:[0,1,1]
	v_pk_fma_f32 v[8:9], v[14:15], v[12:13], v[8:9] op_sel_hi:[0,1,1]
	v_pk_fma_f32 v[2:3], v[14:15], v[18:19], v[2:3] op_sel_hi:[0,1,1]
	v_pk_fma_f32 v[4:5], v[14:15], v[20:21], v[4:5] op_sel_hi:[0,1,1]
	s_waitcnt lgkmcnt(0)
	v_pk_fma_f32 v[6:7], v[216:217], v[208:209], v[6:7] op_sel_hi:[0,1,1]
	v_pk_fma_f32 v[8:9], v[216:217], v[210:211], v[8:9] op_sel_hi:[0,1,1]
	v_pk_fma_f32 v[2:3], v[216:217], v[212:213], v[2:3] op_sel_hi:[0,1,1]
	v_pk_fma_f32 v[4:5], v[216:217], v[214:215], v[4:5] op_sel_hi:[0,1,1]
	v_mov_b32_e32 v1, v244
	s_waitcnt vmcnt(0)
	v_mul_f32_e32 v1, v6, v1
	v_and_b32_e32 v6, 0x7fffffff, v1
	v_cmp_nlt_f32_e64 s[6:7], |v1|, s37
	s_and_saveexec_b64 s[8:9], s[6:7]
	s_xor_b64 s[12:13], exec, s[8:9]
	s_cbranch_execz .LBB0_432
	v_lshrrev_b32_e32 v10, 23, v6
	v_add_u32_e32 v10, 0xffffff88, v10
	v_cmp_lt_u32_e32 vcc, 63, v10
	s_nop 1
	v_cndmask_b32_e32 v11, 0, v145, vcc
	v_add_u32_e32 v10, v11, v10
	v_cmp_lt_u32_e64 s[6:7], 31, v10
	s_nop 1
	v_cndmask_b32_e64 v11, 0, v146, s[6:7]
	v_add_u32_e32 v10, v11, v10
	v_cmp_lt_u32_e64 s[8:9], 31, v10
	s_nop 1
	v_cndmask_b32_e64 v11, 0, v146, s[8:9]
	v_add_u32_e32 v16, v11, v10
	v_and_b32_e32 v10, 0x7fffff, v6
	v_or_b32_e32 v24, 0x800000, v10
	v_mad_u64_u32 v[10:11], s[10:11], v24, s38, 0
	v_mov_b32_e32 v62, v11
	v_mad_u64_u32 v[12:13], s[10:11], v24, s39, v[62:63]
	v_mov_b32_e32 v62, v13
	v_mad_u64_u32 v[14:15], s[10:11], v24, s40, v[62:63]
	v_mov_b32_e32 v62, v15
	v_mad_u64_u32 v[18:19], s[10:11], v24, s41, v[62:63]
	v_mov_b32_e32 v62, v19
	v_mad_u64_u32 v[20:21], s[10:11], v24, s42, v[62:63]
	v_mov_b32_e32 v62, v21
	v_mad_u64_u32 v[22:23], s[10:11], v24, s43, v[62:63]
	v_mov_b32_e32 v62, v23
	v_mad_u64_u32 v[24:25], s[10:11], v24, s44, v[62:63]
	v_cndmask_b32_e32 v11, v22, v18, vcc
	v_cndmask_b32_e32 v13, v24, v20, vcc
	v_cndmask_b32_e32 v19, v25, v22, vcc
	v_cndmask_b32_e64 v15, v13, v11, s[6:7]
	v_cndmask_b32_e64 v13, v19, v13, s[6:7]
	v_cndmask_b32_e32 v19, v20, v14, vcc
	v_cndmask_b32_e64 v11, v11, v19, s[6:7]
	v_cndmask_b32_e32 v12, v18, v12, vcc
	v_cndmask_b32_e64 v13, v13, v15, s[8:9]
	v_cndmask_b32_e64 v15, v15, v11, s[8:9]
	v_sub_u32_e32 v20, 32, v16
	v_cmp_eq_u32_e64 s[10:11], 0, v16
	v_cndmask_b32_e64 v16, v19, v12, s[6:7]
	v_alignbit_b32 v21, v13, v15, v20
	v_cndmask_b32_e64 v11, v11, v16, s[8:9]
	v_cndmask_b32_e64 v13, v21, v13, s[10:11]
	v_alignbit_b32 v18, v15, v11, v20
	v_cndmask_b32_e32 v10, v14, v10, vcc
	v_cndmask_b32_e64 v15, v18, v15, s[10:11]
	v_bfe_u32 v21, v13, 29, 1
	v_cndmask_b32_e64 v10, v12, v10, s[6:7]
	v_alignbit_b32 v18, v13, v15, 30
	v_sub_u32_e32 v22, 0, v21
	v_cndmask_b32_e64 v10, v16, v10, s[8:9]
	v_xor_b32_e32 v18, v18, v22
	v_alignbit_b32 v12, v11, v10, v20
	v_cndmask_b32_e64 v11, v12, v11, s[10:11]
	v_ffbh_u32_e32 v14, v18
	v_alignbit_b32 v12, v15, v11, 30
	v_min_u32_e32 v14, 32, v14
	v_alignbit_b32 v10, v11, v10, 30
	v_xor_b32_e32 v12, v12, v22
	v_sub_u32_e32 v15, 31, v14
	v_xor_b32_e32 v10, v10, v22
	v_alignbit_b32 v16, v18, v12, v15
	v_alignbit_b32 v10, v12, v10, v15
	v_alignbit_b32 v11, v16, v10, 9
	v_ffbh_u32_e32 v12, v11
	v_min_u32_e32 v12, 32, v12
	v_lshrrev_b32_e32 v19, 29, v13
	v_not_b32_e32 v15, v12
	v_alignbit_b32 v10, v11, v10, v15
	v_lshlrev_b32_e32 v11, 31, v19
	v_or_b32_e32 v15, 0x33000000, v11
	v_add_lshl_u32 v12, v12, v14, 23
	v_lshrrev_b32_e32 v10, 9, v10
	v_sub_u32_e32 v12, v15, v12
	v_or_b32_e32 v11, 0.5, v11
	v_lshlrev_b32_e32 v14, 23, v14
	v_or_b32_e32 v10, v12, v10
	v_lshrrev_b32_e32 v12, 9, v16
	v_sub_u32_e32 v11, v11, v14
	v_or_b32_e32 v11, v12, v11
	v_mul_f32_e32 v12, 0x3fc90fda, v11
	v_fma_f32 v14, v11, s45, -v12
	v_fmac_f32_e32 v14, 0x33a22168, v11
	v_fmac_f32_e32 v14, 0x3fc90fda, v10
	v_lshrrev_b32_e32 v11, 30, v13
	v_add_f32_e32 v10, v12, v14
	v_add_u32_e32 v11, v21, v11
.LBB0_432:
	s_andn2_saveexec_b64 s[6:7], s[12:13]
	v_mul_f32_e64 v10, |v1|, s46
	v_rndne_f32_e32 v12, v10
	v_cvt_i32_f32_e32 v11, v12
	v_fma_f32 v10, v12, s47, |v1|
	v_fmac_f32_e32 v10, 0xb3a22168, v12
	v_fmac_f32_e32 v10, 0xa7c234c4, v12
	s_or_b64 exec, exec, s[6:7]
	v_mov_b32_e32 v12, v245
	v_mul_f32_e32 v13, v10, v10
	v_and_b32_e32 v14, 1, v11
	v_lshlrev_b32_e32 v11, 30, v11
	v_fmamk_f32 v15, v13, 0xb94c1982, v125
	v_fmamk_f32 v16, v13, 0x37d75334, v143
	v_xor_b32_e32 v6, v6, v1
	v_and_b32_e32 v11, 0x80000000, v11
	v_fmaak_f32 v15, v13, v15, 0xbe2aaa9d
	v_fmaak_f32 v16, v13, v16, 0x3d2aabf7
	v_xor_b32_e32 v6, v6, v11
	v_mul_f32_e32 v11, v13, v15
	v_fmaak_f32 v15, v13, v16, 0xbf000004
	v_fmac_f32_e32 v10, v10, v11
	v_fma_f32 v11, v13, v15, 1.0
	v_cmp_eq_u32_e32 vcc, 0, v14
	s_nop 1
	v_cndmask_b32_e32 v10, v11, v10, vcc
	v_xor_b32_e32 v6, v6, v10
	v_cmp_class_f32_e64 vcc, v1, s49
	s_nop 1
	v_cndmask_b32_e32 v1, v147, v6, vcc
	ds_write_b32 v134, v1 offset:25856
	s_waitcnt vmcnt(0)
	v_mul_f32_e32 v1, v7, v12
	v_and_b32_e32 v6, 0x7fffffff, v1
	v_cmp_nlt_f32_e64 s[6:7], |v1|, s37
	s_and_saveexec_b64 s[8:9], s[6:7]
	s_xor_b64 s[12:13], exec, s[8:9]
	s_cbranch_execz .LBB0_436
	v_lshrrev_b32_e32 v7, 23, v6
	v_add_u32_e32 v7, 0xffffff88, v7
	v_cmp_lt_u32_e32 vcc, 63, v7
	s_nop 1
	v_cndmask_b32_e32 v10, 0, v145, vcc
	v_add_u32_e32 v7, v10, v7
	v_cmp_lt_u32_e64 s[6:7], 31, v7
	s_nop 1
	v_cndmask_b32_e64 v10, 0, v146, s[6:7]
	v_add_u32_e32 v7, v10, v7
	v_cmp_lt_u32_e64 s[8:9], 31, v7
	s_nop 1
	v_cndmask_b32_e64 v10, 0, v146, s[8:9]
	v_add_u32_e32 v7, v10, v7
	v_and_b32_e32 v10, 0x7fffff, v6
	v_or_b32_e32 v16, 0x800000, v10
	v_mad_u64_u32 v[10:11], s[10:11], v16, s38, 0
	v_mov_b32_e32 v62, v11
	v_mad_u64_u32 v[12:13], s[10:11], v16, s39, v[62:63]
	v_mov_b32_e32 v62, v13
	v_mad_u64_u32 v[14:15], s[10:11], v16, s40, v[62:63]
	v_mov_b32_e32 v62, v15
	v_mad_u64_u32 v[18:19], s[10:11], v16, s41, v[62:63]
	v_mov_b32_e32 v62, v19
	v_mad_u64_u32 v[20:21], s[10:11], v16, s42, v[62:63]
	v_mov_b32_e32 v62, v21
	v_mad_u64_u32 v[22:23], s[10:11], v16, s43, v[62:63]
	v_mov_b32_e32 v62, v23
	v_mad_u64_u32 v[24:25], s[10:11], v16, s44, v[62:63]
	v_cndmask_b32_e32 v11, v22, v18, vcc
	v_cndmask_b32_e32 v13, v24, v20, vcc
	v_cndmask_b32_e32 v16, v25, v22, vcc
	v_cndmask_b32_e64 v15, v13, v11, s[6:7]
	v_cndmask_b32_e64 v13, v16, v13, s[6:7]
	v_cndmask_b32_e32 v16, v20, v14, vcc
	v_cndmask_b32_e64 v11, v11, v16, s[6:7]
	v_sub_u32_e32 v19, 32, v7
	v_cmp_eq_u32_e64 s[10:11], 0, v7
	v_cndmask_b32_e32 v7, v18, v12, vcc
	v_cndmask_b32_e64 v13, v13, v15, s[8:9]
	v_cndmask_b32_e64 v15, v15, v11, s[8:9]
	v_cndmask_b32_e64 v12, v16, v7, s[6:7]
	v_alignbit_b32 v20, v13, v15, v19
	v_cndmask_b32_e64 v11, v11, v12, s[8:9]
	v_cndmask_b32_e64 v13, v20, v13, s[10:11]
	v_alignbit_b32 v16, v15, v11, v19
	v_cndmask_b32_e32 v10, v14, v10, vcc
	v_cndmask_b32_e64 v15, v16, v15, s[10:11]
	v_bfe_u32 v20, v13, 29, 1
	v_cndmask_b32_e64 v7, v7, v10, s[6:7]
	v_alignbit_b32 v16, v13, v15, 30
	v_sub_u32_e32 v21, 0, v20
	v_cndmask_b32_e64 v7, v12, v7, s[8:9]
	v_xor_b32_e32 v16, v16, v21
	v_alignbit_b32 v10, v11, v7, v19
	v_cndmask_b32_e64 v10, v10, v11, s[10:11]
	v_ffbh_u32_e32 v12, v16
	v_alignbit_b32 v11, v15, v10, 30
	v_min_u32_e32 v12, 32, v12
	v_alignbit_b32 v7, v10, v7, 30
	v_xor_b32_e32 v11, v11, v21
	v_sub_u32_e32 v14, 31, v12
	v_xor_b32_e32 v7, v7, v21
	v_alignbit_b32 v15, v16, v11, v14
	v_alignbit_b32 v7, v11, v7, v14
	v_alignbit_b32 v10, v15, v7, 9
	v_ffbh_u32_e32 v11, v10
	v_min_u32_e32 v11, 32, v11
	v_lshrrev_b32_e32 v18, 29, v13
	v_not_b32_e32 v14, v11
	v_alignbit_b32 v7, v10, v7, v14
	v_lshlrev_b32_e32 v10, 31, v18
	v_or_b32_e32 v14, 0x33000000, v10
	v_add_lshl_u32 v11, v11, v12, 23
	v_lshrrev_b32_e32 v7, 9, v7
	v_sub_u32_e32 v11, v14, v11
	v_or_b32_e32 v10, 0.5, v10
	v_lshlrev_b32_e32 v12, 23, v12
	v_or_b32_e32 v7, v11, v7
	v_lshrrev_b32_e32 v11, 9, v15
	v_sub_u32_e32 v10, v10, v12
	v_or_b32_e32 v10, v11, v10
	v_mul_f32_e32 v11, 0x3fc90fda, v10
	v_fma_f32 v12, v10, s45, -v11
	v_fmac_f32_e32 v12, 0x33a22168, v10
	v_fmac_f32_e32 v12, 0x3fc90fda, v7
	v_lshrrev_b32_e32 v10, 30, v13
	v_add_f32_e32 v7, v11, v12
	v_add_u32_e32 v10, v20, v10
.LBB0_436:
	s_andn2_saveexec_b64 s[6:7], s[12:13]
	v_mul_f32_e64 v7, |v1|, s46
	v_rndne_f32_e32 v11, v7
	v_cvt_i32_f32_e32 v10, v11
	v_fma_f32 v7, v11, s47, |v1|
	v_fmac_f32_e32 v7, 0xb3a22168, v11
	v_fmac_f32_e32 v7, 0xa7c234c4, v11
	s_or_b64 exec, exec, s[6:7]
	v_mov_b32_e32 v11, v246
	v_mul_f32_e32 v12, v7, v7
	v_and_b32_e32 v13, 1, v10
	v_lshlrev_b32_e32 v10, 30, v10
	v_fmamk_f32 v14, v12, 0xb94c1982, v125
	v_fmamk_f32 v15, v12, 0x37d75334, v143
	v_xor_b32_e32 v6, v6, v1
	v_and_b32_e32 v10, 0x80000000, v10
	v_fmaak_f32 v14, v12, v14, 0xbe2aaa9d
	v_fmaak_f32 v15, v12, v15, 0x3d2aabf7
	v_xor_b32_e32 v6, v6, v10
	v_mul_f32_e32 v10, v12, v14
	v_fmaak_f32 v14, v12, v15, 0xbf000004
	v_fmac_f32_e32 v7, v7, v10
	v_fma_f32 v10, v12, v14, 1.0
	v_cmp_eq_u32_e32 vcc, 0, v13
	s_nop 1
	v_cndmask_b32_e32 v7, v10, v7, vcc
	v_xor_b32_e32 v6, v6, v7
	v_cmp_class_f32_e64 vcc, v1, s49
	s_nop 1
	v_cndmask_b32_e32 v1, v147, v6, vcc
	ds_write_b32 v134, v1 offset:25860
	s_waitcnt vmcnt(0)
	v_mul_f32_e32 v1, v8, v11
	v_and_b32_e32 v6, 0x7fffffff, v1
	v_cmp_nlt_f32_e64 s[6:7], |v1|, s37
	s_and_saveexec_b64 s[8:9], s[6:7]
	s_xor_b64 s[12:13], exec, s[8:9]
	s_cbranch_execz .LBB0_440
	v_lshrrev_b32_e32 v7, 23, v6
	v_add_u32_e32 v7, 0xffffff88, v7
	v_cmp_lt_u32_e32 vcc, 63, v7
	s_nop 1
	v_cndmask_b32_e32 v8, 0, v145, vcc
	v_add_u32_e32 v7, v8, v7
	v_cmp_lt_u32_e64 s[6:7], 31, v7
	s_nop 1
	v_cndmask_b32_e64 v8, 0, v146, s[6:7]
	v_add_u32_e32 v7, v8, v7
	v_cmp_lt_u32_e64 s[8:9], 31, v7
	s_nop 1
	v_cndmask_b32_e64 v8, 0, v146, s[8:9]
	v_add_u32_e32 v7, v8, v7
	v_and_b32_e32 v8, 0x7fffff, v6
	v_or_b32_e32 v8, 0x800000, v8
	v_mad_u64_u32 v[10:11], s[10:11], v8, s38, 0
	v_mov_b32_e32 v62, v11
	v_mad_u64_u32 v[12:13], s[10:11], v8, s39, v[62:63]
	v_mov_b32_e32 v62, v13
	v_mad_u64_u32 v[14:15], s[10:11], v8, s40, v[62:63]
	v_mov_b32_e32 v62, v15
	v_mad_u64_u32 v[18:19], s[10:11], v8, s41, v[62:63]
	v_mov_b32_e32 v62, v19
	v_mad_u64_u32 v[20:21], s[10:11], v8, s42, v[62:63]
	v_mov_b32_e32 v62, v21
	v_mad_u64_u32 v[22:23], s[10:11], v8, s43, v[62:63]
	v_mov_b32_e32 v62, v23
	v_mad_u64_u32 v[24:25], s[10:11], v8, s44, v[62:63]
	v_cndmask_b32_e32 v11, v22, v18, vcc
	v_cndmask_b32_e32 v8, v24, v20, vcc
	v_cndmask_b32_e32 v15, v25, v22, vcc
	v_cndmask_b32_e64 v13, v8, v11, s[6:7]
	v_cndmask_b32_e64 v8, v15, v8, s[6:7]
	v_cndmask_b32_e32 v15, v20, v14, vcc
	v_cndmask_b32_e64 v11, v11, v15, s[6:7]
	v_sub_u32_e32 v16, 32, v7
	v_cmp_eq_u32_e64 s[10:11], 0, v7
	v_cndmask_b32_e32 v7, v18, v12, vcc
	v_cndmask_b32_e64 v8, v8, v13, s[8:9]
	v_cndmask_b32_e64 v13, v13, v11, s[8:9]
	v_cndmask_b32_e64 v12, v15, v7, s[6:7]
	v_alignbit_b32 v19, v8, v13, v16
	v_cndmask_b32_e64 v11, v11, v12, s[8:9]
	v_cndmask_b32_e64 v8, v19, v8, s[10:11]
	v_alignbit_b32 v15, v13, v11, v16
	v_cndmask_b32_e32 v10, v14, v10, vcc
	v_cndmask_b32_e64 v13, v15, v13, s[10:11]
	v_bfe_u32 v19, v8, 29, 1
	v_cndmask_b32_e64 v7, v7, v10, s[6:7]
	v_alignbit_b32 v15, v8, v13, 30
	v_sub_u32_e32 v20, 0, v19
	v_cndmask_b32_e64 v7, v12, v7, s[8:9]
	v_xor_b32_e32 v15, v15, v20
	v_alignbit_b32 v10, v11, v7, v16
	v_cndmask_b32_e64 v10, v10, v11, s[10:11]
	v_ffbh_u32_e32 v12, v15
	v_alignbit_b32 v11, v13, v10, 30
	v_min_u32_e32 v12, 32, v12
	v_alignbit_b32 v7, v10, v7, 30
	v_xor_b32_e32 v11, v11, v20
	v_sub_u32_e32 v13, 31, v12
	v_xor_b32_e32 v7, v7, v20
	v_alignbit_b32 v14, v15, v11, v13
	v_alignbit_b32 v7, v11, v7, v13
	v_alignbit_b32 v10, v14, v7, 9
	v_ffbh_u32_e32 v11, v10
	v_min_u32_e32 v11, 32, v11
	v_lshrrev_b32_e32 v18, 29, v8
	v_not_b32_e32 v13, v11
	v_alignbit_b32 v7, v10, v7, v13
	v_lshlrev_b32_e32 v10, 31, v18
	v_or_b32_e32 v13, 0x33000000, v10
	v_add_lshl_u32 v11, v11, v12, 23
	v_lshrrev_b32_e32 v7, 9, v7
	v_sub_u32_e32 v11, v13, v11
	v_or_b32_e32 v10, 0.5, v10
	v_lshlrev_b32_e32 v12, 23, v12
	v_or_b32_e32 v7, v11, v7
	v_lshrrev_b32_e32 v11, 9, v14
	v_sub_u32_e32 v10, v10, v12
	v_or_b32_e32 v10, v11, v10
	v_mul_f32_e32 v11, 0x3fc90fda, v10
	v_fma_f32 v12, v10, s45, -v11
	v_fmac_f32_e32 v12, 0x33a22168, v10
	v_fmac_f32_e32 v12, 0x3fc90fda, v7
	v_lshrrev_b32_e32 v8, 30, v8
	v_add_f32_e32 v7, v11, v12
	v_add_u32_e32 v8, v19, v8
.LBB0_440:
	s_andn2_saveexec_b64 s[6:7], s[12:13]
	v_mul_f32_e64 v7, |v1|, s46
	v_rndne_f32_e32 v10, v7
	v_cvt_i32_f32_e32 v8, v10
	v_fma_f32 v7, v10, s47, |v1|
	v_fmac_f32_e32 v7, 0xb3a22168, v10
	v_fmac_f32_e32 v7, 0xa7c234c4, v10
	s_or_b64 exec, exec, s[6:7]
	v_mov_b32_e32 v10, v247
	v_mul_f32_e32 v11, v7, v7
	v_and_b32_e32 v12, 1, v8
	v_lshlrev_b32_e32 v8, 30, v8
	v_fmamk_f32 v13, v11, 0xb94c1982, v125
	v_fmamk_f32 v14, v11, 0x37d75334, v143
	v_xor_b32_e32 v6, v6, v1
	v_and_b32_e32 v8, 0x80000000, v8
	v_fmaak_f32 v13, v11, v13, 0xbe2aaa9d
	v_fmaak_f32 v14, v11, v14, 0x3d2aabf7
	v_xor_b32_e32 v6, v6, v8
	v_mul_f32_e32 v8, v11, v13
	v_fmaak_f32 v13, v11, v14, 0xbf000004
	v_fmac_f32_e32 v7, v7, v8
	v_fma_f32 v8, v11, v13, 1.0
	v_cmp_eq_u32_e32 vcc, 0, v12
	s_nop 1
	v_cndmask_b32_e32 v7, v8, v7, vcc
	v_xor_b32_e32 v6, v6, v7
	v_cmp_class_f32_e64 vcc, v1, s49
	s_nop 1
	v_cndmask_b32_e32 v1, v147, v6, vcc
	ds_write_b32 v134, v1 offset:25864
	s_waitcnt vmcnt(0)
	v_mul_f32_e32 v1, v9, v10
	v_and_b32_e32 v6, 0x7fffffff, v1
	v_cmp_nlt_f32_e64 s[6:7], |v1|, s37
	s_and_saveexec_b64 s[8:9], s[6:7]
	s_xor_b64 s[12:13], exec, s[8:9]
	s_cbranch_execz .LBB0_444
	v_lshrrev_b32_e32 v7, 23, v6
	v_add_u32_e32 v7, 0xffffff88, v7
	v_cmp_lt_u32_e32 vcc, 63, v7
	s_nop 1
	v_cndmask_b32_e32 v8, 0, v145, vcc
	v_add_u32_e32 v7, v8, v7
	v_cmp_lt_u32_e64 s[6:7], 31, v7
	s_nop 1
	v_cndmask_b32_e64 v8, 0, v146, s[6:7]
	v_add_u32_e32 v7, v8, v7
	v_cmp_lt_u32_e64 s[8:9], 31, v7
	s_nop 1
	v_cndmask_b32_e64 v8, 0, v146, s[8:9]
	v_add_u32_e32 v7, v8, v7
	v_and_b32_e32 v8, 0x7fffff, v6
	v_or_b32_e32 v16, 0x800000, v8
	v_mad_u64_u32 v[8:9], s[10:11], v16, s38, 0
	v_mov_b32_e32 v62, v9
	v_mad_u64_u32 v[10:11], s[10:11], v16, s39, v[62:63]
	v_mov_b32_e32 v62, v11
	v_mad_u64_u32 v[12:13], s[10:11], v16, s40, v[62:63]
	v_mov_b32_e32 v62, v13
	v_mad_u64_u32 v[14:15], s[10:11], v16, s41, v[62:63]
	v_mov_b32_e32 v62, v15
	v_mad_u64_u32 v[18:19], s[10:11], v16, s42, v[62:63]
	v_mov_b32_e32 v62, v19
	v_mad_u64_u32 v[20:21], s[10:11], v16, s43, v[62:63]
	v_mov_b32_e32 v62, v21
	v_mad_u64_u32 v[22:23], s[10:11], v16, s44, v[62:63]
	v_cndmask_b32_e32 v9, v20, v14, vcc
	v_cndmask_b32_e32 v11, v22, v18, vcc
	v_cndmask_b32_e32 v15, v23, v20, vcc
	v_cndmask_b32_e64 v13, v11, v9, s[6:7]
	v_cndmask_b32_e64 v11, v15, v11, s[6:7]
	v_cndmask_b32_e32 v15, v18, v12, vcc
	v_cndmask_b32_e64 v9, v9, v15, s[6:7]
	v_sub_u32_e32 v16, 32, v7
	v_cmp_eq_u32_e64 s[10:11], 0, v7
	v_cndmask_b32_e32 v7, v14, v10, vcc
	v_cndmask_b32_e64 v11, v11, v13, s[8:9]
	v_cndmask_b32_e64 v13, v13, v9, s[8:9]
	v_cndmask_b32_e64 v10, v15, v7, s[6:7]
	v_alignbit_b32 v18, v11, v13, v16
	v_cndmask_b32_e64 v9, v9, v10, s[8:9]
	v_cndmask_b32_e64 v11, v18, v11, s[10:11]
	v_alignbit_b32 v14, v13, v9, v16
	v_cndmask_b32_e32 v8, v12, v8, vcc
	v_cndmask_b32_e64 v13, v14, v13, s[10:11]
	v_bfe_u32 v18, v11, 29, 1
	v_cndmask_b32_e64 v7, v7, v8, s[6:7]
	v_alignbit_b32 v14, v11, v13, 30
	v_sub_u32_e32 v19, 0, v18
	v_cndmask_b32_e64 v7, v10, v7, s[8:9]
	v_xor_b32_e32 v14, v14, v19
	v_alignbit_b32 v8, v9, v7, v16
	v_cndmask_b32_e64 v8, v8, v9, s[10:11]
	v_ffbh_u32_e32 v10, v14
	v_alignbit_b32 v9, v13, v8, 30
	v_min_u32_e32 v10, 32, v10
	v_alignbit_b32 v7, v8, v7, 30
	v_xor_b32_e32 v9, v9, v19
	v_sub_u32_e32 v12, 31, v10
	v_xor_b32_e32 v7, v7, v19
	v_alignbit_b32 v13, v14, v9, v12
	v_alignbit_b32 v7, v9, v7, v12
	v_alignbit_b32 v8, v13, v7, 9
	v_ffbh_u32_e32 v9, v8
	v_min_u32_e32 v9, 32, v9
	v_lshrrev_b32_e32 v15, 29, v11
	v_not_b32_e32 v12, v9
	v_alignbit_b32 v7, v8, v7, v12
	v_lshlrev_b32_e32 v8, 31, v15
	v_or_b32_e32 v12, 0x33000000, v8
	v_add_lshl_u32 v9, v9, v10, 23
	v_lshrrev_b32_e32 v7, 9, v7
	v_sub_u32_e32 v9, v12, v9
	v_or_b32_e32 v8, 0.5, v8
	v_lshlrev_b32_e32 v10, 23, v10
	v_or_b32_e32 v7, v9, v7
	v_lshrrev_b32_e32 v9, 9, v13
	v_sub_u32_e32 v8, v8, v10
	v_or_b32_e32 v8, v9, v8
	v_mul_f32_e32 v9, 0x3fc90fda, v8
	v_fma_f32 v10, v8, s45, -v9
	v_fmac_f32_e32 v10, 0x33a22168, v8
	v_fmac_f32_e32 v10, 0x3fc90fda, v7
	v_lshrrev_b32_e32 v8, 30, v11
	v_add_f32_e32 v7, v9, v10
	v_add_u32_e32 v8, v18, v8
.LBB0_444:
	s_andn2_saveexec_b64 s[6:7], s[12:13]
	v_mul_f32_e64 v7, |v1|, s46
	v_rndne_f32_e32 v9, v7
	v_cvt_i32_f32_e32 v8, v9
	v_fma_f32 v7, v9, s47, |v1|
	v_fmac_f32_e32 v7, 0xb3a22168, v9
	v_fmac_f32_e32 v7, 0xa7c234c4, v9
	s_or_b64 exec, exec, s[6:7]
	v_mov_b32_e32 v9, v248
	v_mul_f32_e32 v10, v7, v7
	v_and_b32_e32 v11, 1, v8
	v_lshlrev_b32_e32 v8, 30, v8
	v_fmamk_f32 v12, v10, 0xb94c1982, v125
	v_fmamk_f32 v13, v10, 0x37d75334, v143
	v_xor_b32_e32 v6, v6, v1
	v_and_b32_e32 v8, 0x80000000, v8
	v_fmaak_f32 v12, v10, v12, 0xbe2aaa9d
	v_fmaak_f32 v13, v10, v13, 0x3d2aabf7
	v_xor_b32_e32 v6, v6, v8
	v_mul_f32_e32 v8, v10, v12
	v_fmaak_f32 v12, v10, v13, 0xbf000004
	v_fmac_f32_e32 v7, v7, v8
	v_fma_f32 v8, v10, v12, 1.0
	v_cmp_eq_u32_e32 vcc, 0, v11
	s_nop 1
	v_cndmask_b32_e32 v7, v8, v7, vcc
	v_xor_b32_e32 v6, v6, v7
	v_cmp_class_f32_e64 vcc, v1, s49
	s_nop 1
	v_cndmask_b32_e32 v1, v147, v6, vcc
	ds_write_b32 v134, v1 offset:25868
	s_waitcnt vmcnt(0)
	v_mul_f32_e32 v1, v2, v9
	v_and_b32_e32 v2, 0x7fffffff, v1
	v_cmp_nlt_f32_e64 s[6:7], |v1|, s37
	s_and_saveexec_b64 s[8:9], s[6:7]
	s_xor_b64 s[12:13], exec, s[8:9]
	s_cbranch_execz .LBB0_448
	v_lshrrev_b32_e32 v6, 23, v2
	v_add_u32_e32 v6, 0xffffff88, v6
	v_cmp_lt_u32_e32 vcc, 63, v6
	s_nop 1
	v_cndmask_b32_e32 v7, 0, v145, vcc
	v_add_u32_e32 v6, v7, v6
	v_cmp_lt_u32_e64 s[6:7], 31, v6
	s_nop 1
	v_cndmask_b32_e64 v7, 0, v146, s[6:7]
	v_add_u32_e32 v6, v7, v6
	v_cmp_lt_u32_e64 s[8:9], 31, v6
	s_nop 1
	v_cndmask_b32_e64 v7, 0, v146, s[8:9]
	v_add_u32_e32 v16, v7, v6
	v_and_b32_e32 v6, 0x7fffff, v2
	v_or_b32_e32 v20, 0x800000, v6
	v_mad_u64_u32 v[6:7], s[10:11], v20, s38, 0
	v_mov_b32_e32 v62, v7
	v_mad_u64_u32 v[8:9], s[10:11], v20, s39, v[62:63]
	v_mov_b32_e32 v62, v9
	v_mad_u64_u32 v[10:11], s[10:11], v20, s40, v[62:63]
	v_mov_b32_e32 v62, v11
	v_mad_u64_u32 v[12:13], s[10:11], v20, s41, v[62:63]
	v_mov_b32_e32 v62, v13
	v_mad_u64_u32 v[14:15], s[10:11], v20, s42, v[62:63]
	v_mov_b32_e32 v62, v15
	v_mad_u64_u32 v[18:19], s[10:11], v20, s43, v[62:63]
	v_mov_b32_e32 v62, v19
	v_mad_u64_u32 v[20:21], s[10:11], v20, s44, v[62:63]
	v_cndmask_b32_e32 v7, v18, v12, vcc
	v_cndmask_b32_e32 v9, v20, v14, vcc
	v_cndmask_b32_e32 v13, v21, v18, vcc
	v_cndmask_b32_e64 v11, v9, v7, s[6:7]
	v_cndmask_b32_e64 v9, v13, v9, s[6:7]
	v_cndmask_b32_e32 v13, v14, v10, vcc
	v_cndmask_b32_e64 v7, v7, v13, s[6:7]
	v_cndmask_b32_e32 v8, v12, v8, vcc
	v_cndmask_b32_e64 v9, v9, v11, s[8:9]
	v_cndmask_b32_e64 v11, v11, v7, s[8:9]
	v_sub_u32_e32 v14, 32, v16
	v_cndmask_b32_e64 v12, v13, v8, s[6:7]
	v_alignbit_b32 v15, v9, v11, v14
	v_cmp_eq_u32_e64 s[10:11], 0, v16
	v_cndmask_b32_e64 v7, v7, v12, s[8:9]
	v_alignbit_b32 v13, v11, v7, v14
	v_cndmask_b32_e64 v9, v15, v9, s[10:11]
	v_cndmask_b32_e32 v6, v10, v6, vcc
	v_cndmask_b32_e64 v11, v13, v11, s[10:11]
	v_bfe_u32 v16, v9, 29, 1
	v_cndmask_b32_e64 v6, v8, v6, s[6:7]
	v_alignbit_b32 v13, v9, v11, 30
	v_sub_u32_e32 v18, 0, v16
	v_cndmask_b32_e64 v6, v12, v6, s[8:9]
	v_xor_b32_e32 v13, v13, v18
	v_alignbit_b32 v8, v7, v6, v14
	v_cndmask_b32_e64 v7, v8, v7, s[10:11]
	v_ffbh_u32_e32 v10, v13
	v_alignbit_b32 v8, v11, v7, 30
	v_min_u32_e32 v10, 32, v10
	v_alignbit_b32 v6, v7, v6, 30
	v_xor_b32_e32 v8, v8, v18
	v_sub_u32_e32 v11, 31, v10
	v_xor_b32_e32 v6, v6, v18
	v_alignbit_b32 v12, v13, v8, v11
	v_alignbit_b32 v6, v8, v6, v11
	v_alignbit_b32 v7, v12, v6, 9
	v_ffbh_u32_e32 v8, v7
	v_min_u32_e32 v8, 32, v8
	v_lshrrev_b32_e32 v15, 29, v9
	v_not_b32_e32 v11, v8
	v_alignbit_b32 v6, v7, v6, v11
	v_lshlrev_b32_e32 v7, 31, v15
	v_or_b32_e32 v11, 0x33000000, v7
	v_add_lshl_u32 v8, v8, v10, 23
	v_lshrrev_b32_e32 v6, 9, v6
	v_sub_u32_e32 v8, v11, v8
	v_or_b32_e32 v7, 0.5, v7
	v_lshlrev_b32_e32 v10, 23, v10
	v_or_b32_e32 v6, v8, v6
	v_lshrrev_b32_e32 v8, 9, v12
	v_sub_u32_e32 v7, v7, v10
	v_or_b32_e32 v7, v8, v7
	v_mul_f32_e32 v8, 0x3fc90fda, v7
	v_fma_f32 v10, v7, s45, -v8
	v_fmac_f32_e32 v10, 0x33a22168, v7
	v_fmac_f32_e32 v10, 0x3fc90fda, v6
	v_lshrrev_b32_e32 v7, 30, v9
	v_add_f32_e32 v6, v8, v10
	v_add_u32_e32 v7, v16, v7
.LBB0_448:
	s_andn2_saveexec_b64 s[6:7], s[12:13]
	v_mul_f32_e64 v6, |v1|, s46
	v_rndne_f32_e32 v8, v6
	v_cvt_i32_f32_e32 v7, v8
	v_fma_f32 v6, v8, s47, |v1|
	v_fmac_f32_e32 v6, 0xb3a22168, v8
	v_fmac_f32_e32 v6, 0xa7c234c4, v8
	s_or_b64 exec, exec, s[6:7]
	v_mov_b32_e32 v8, v249
	v_mul_f32_e32 v9, v6, v6
	v_and_b32_e32 v10, 1, v7
	v_lshlrev_b32_e32 v7, 30, v7
	v_fmamk_f32 v11, v9, 0xb94c1982, v125
	v_fmamk_f32 v12, v9, 0x37d75334, v143
	v_xor_b32_e32 v2, v2, v1
	v_and_b32_e32 v7, 0x80000000, v7
	v_fmaak_f32 v11, v9, v11, 0xbe2aaa9d
	v_fmaak_f32 v12, v9, v12, 0x3d2aabf7
	v_xor_b32_e32 v2, v2, v7
	v_mul_f32_e32 v7, v9, v11
	v_fmaak_f32 v11, v9, v12, 0xbf000004
	v_fmac_f32_e32 v6, v6, v7
	v_fma_f32 v7, v9, v11, 1.0
	v_cmp_eq_u32_e32 vcc, 0, v10
	s_nop 1
	v_cndmask_b32_e32 v6, v7, v6, vcc
	v_xor_b32_e32 v2, v2, v6
	v_cmp_class_f32_e64 vcc, v1, s49
	s_nop 1
	v_cndmask_b32_e32 v1, v147, v2, vcc
	ds_write_b32 v134, v1 offset:25872
	s_waitcnt vmcnt(0)
	v_mul_f32_e32 v1, v3, v8
	v_and_b32_e32 v2, 0x7fffffff, v1
	v_cmp_nlt_f32_e64 s[6:7], |v1|, s37
	s_and_saveexec_b64 s[8:9], s[6:7]
	s_xor_b64 s[12:13], exec, s[8:9]
	s_cbranch_execz .LBB0_452
	v_lshrrev_b32_e32 v3, 23, v2
	v_add_u32_e32 v3, 0xffffff88, v3
	v_cmp_lt_u32_e32 vcc, 63, v3
	s_nop 1
	v_cndmask_b32_e32 v6, 0, v145, vcc
	v_add_u32_e32 v3, v6, v3
	v_cmp_lt_u32_e64 s[6:7], 31, v3
	s_nop 1
	v_cndmask_b32_e64 v6, 0, v146, s[6:7]
	v_add_u32_e32 v3, v6, v3
	v_cmp_lt_u32_e64 s[8:9], 31, v3
	s_nop 1
	v_cndmask_b32_e64 v6, 0, v146, s[8:9]
	v_add_u32_e32 v3, v6, v3
	v_and_b32_e32 v6, 0x7fffff, v2
	v_or_b32_e32 v16, 0x800000, v6
	v_mad_u64_u32 v[6:7], s[10:11], v16, s38, 0
	v_mov_b32_e32 v62, v7
	v_mad_u64_u32 v[8:9], s[10:11], v16, s39, v[62:63]
	v_mov_b32_e32 v62, v9
	v_mad_u64_u32 v[10:11], s[10:11], v16, s40, v[62:63]
	v_mov_b32_e32 v62, v11
	v_mad_u64_u32 v[12:13], s[10:11], v16, s41, v[62:63]
	v_mov_b32_e32 v62, v13
	v_mad_u64_u32 v[14:15], s[10:11], v16, s42, v[62:63]
	v_mov_b32_e32 v62, v15
	v_mad_u64_u32 v[18:19], s[10:11], v16, s43, v[62:63]
	v_mov_b32_e32 v62, v19
	v_mad_u64_u32 v[20:21], s[10:11], v16, s44, v[62:63]
	v_cndmask_b32_e32 v7, v18, v12, vcc
	v_cndmask_b32_e32 v9, v20, v14, vcc
	v_cndmask_b32_e32 v13, v21, v18, vcc
	v_cndmask_b32_e64 v11, v9, v7, s[6:7]
	v_cndmask_b32_e64 v9, v13, v9, s[6:7]
	v_cndmask_b32_e32 v13, v14, v10, vcc
	v_cndmask_b32_e64 v7, v7, v13, s[6:7]
	v_sub_u32_e32 v14, 32, v3
	v_cmp_eq_u32_e64 s[10:11], 0, v3
	v_cndmask_b32_e32 v3, v12, v8, vcc
	v_cndmask_b32_e64 v9, v9, v11, s[8:9]
	v_cndmask_b32_e64 v11, v11, v7, s[8:9]
	v_cndmask_b32_e64 v8, v13, v3, s[6:7]
	v_alignbit_b32 v15, v9, v11, v14
	v_cndmask_b32_e64 v7, v7, v8, s[8:9]
	v_cndmask_b32_e64 v9, v15, v9, s[10:11]
	v_alignbit_b32 v12, v11, v7, v14
	v_cndmask_b32_e32 v6, v10, v6, vcc
	v_cndmask_b32_e64 v11, v12, v11, s[10:11]
	v_bfe_u32 v15, v9, 29, 1
	v_cndmask_b32_e64 v3, v3, v6, s[6:7]
	v_alignbit_b32 v12, v9, v11, 30
	v_sub_u32_e32 v16, 0, v15
	v_cndmask_b32_e64 v3, v8, v3, s[8:9]
	v_xor_b32_e32 v12, v12, v16
	v_alignbit_b32 v6, v7, v3, v14
	v_cndmask_b32_e64 v6, v6, v7, s[10:11]
	v_ffbh_u32_e32 v8, v12
	v_alignbit_b32 v7, v11, v6, 30
	v_min_u32_e32 v8, 32, v8
	v_alignbit_b32 v3, v6, v3, 30
	v_xor_b32_e32 v7, v7, v16
	v_sub_u32_e32 v10, 31, v8
	v_xor_b32_e32 v3, v3, v16
	v_alignbit_b32 v11, v12, v7, v10
	v_alignbit_b32 v3, v7, v3, v10
	v_alignbit_b32 v6, v11, v3, 9
	v_ffbh_u32_e32 v7, v6
	v_min_u32_e32 v7, 32, v7
	v_lshrrev_b32_e32 v13, 29, v9
	v_not_b32_e32 v10, v7
	v_alignbit_b32 v3, v6, v3, v10
	v_lshlrev_b32_e32 v6, 31, v13
	v_or_b32_e32 v10, 0x33000000, v6
	v_add_lshl_u32 v7, v7, v8, 23
	v_lshrrev_b32_e32 v3, 9, v3
	v_sub_u32_e32 v7, v10, v7
	v_or_b32_e32 v6, 0.5, v6
	v_lshlrev_b32_e32 v8, 23, v8
	v_or_b32_e32 v3, v7, v3
	v_lshrrev_b32_e32 v7, 9, v11
	v_sub_u32_e32 v6, v6, v8
	v_or_b32_e32 v6, v7, v6
	v_mul_f32_e32 v7, 0x3fc90fda, v6
	v_fma_f32 v8, v6, s45, -v7
	v_fmac_f32_e32 v8, 0x33a22168, v6
	v_fmac_f32_e32 v8, 0x3fc90fda, v3
	v_lshrrev_b32_e32 v6, 30, v9
	v_add_f32_e32 v3, v7, v8
	v_add_u32_e32 v6, v15, v6
.LBB0_452:
	s_andn2_saveexec_b64 s[6:7], s[12:13]
	v_mul_f32_e64 v3, |v1|, s46
	v_rndne_f32_e32 v7, v3
	v_cvt_i32_f32_e32 v6, v7
	v_fma_f32 v3, v7, s47, |v1|
	v_fmac_f32_e32 v3, 0xb3a22168, v7
	v_fmac_f32_e32 v3, 0xa7c234c4, v7
	s_or_b64 exec, exec, s[6:7]
	v_mov_b32_e32 v7, v250
	v_mul_f32_e32 v8, v3, v3
	v_and_b32_e32 v9, 1, v6
	v_lshlrev_b32_e32 v6, 30, v6
	v_fmamk_f32 v10, v8, 0xb94c1982, v125
	v_fmamk_f32 v11, v8, 0x37d75334, v143
	v_xor_b32_e32 v2, v2, v1
	v_and_b32_e32 v6, 0x80000000, v6
	v_fmaak_f32 v10, v8, v10, 0xbe2aaa9d
	v_fmaak_f32 v11, v8, v11, 0x3d2aabf7
	v_xor_b32_e32 v2, v2, v6
	v_mul_f32_e32 v6, v8, v10
	v_fmaak_f32 v10, v8, v11, 0xbf000004
	v_fmac_f32_e32 v3, v3, v6
	v_fma_f32 v6, v8, v10, 1.0
	v_cmp_eq_u32_e32 vcc, 0, v9
	s_nop 1
	v_cndmask_b32_e32 v3, v6, v3, vcc
	v_xor_b32_e32 v2, v2, v3
	v_cmp_class_f32_e64 vcc, v1, s49
	s_nop 1
	v_cndmask_b32_e32 v1, v147, v2, vcc
	ds_write_b32 v134, v1 offset:25876
	s_waitcnt vmcnt(0)
	v_mul_f32_e32 v1, v4, v7
	v_and_b32_e32 v2, 0x7fffffff, v1
	v_cmp_nlt_f32_e64 s[6:7], |v1|, s37
	s_and_saveexec_b64 s[8:9], s[6:7]
	s_xor_b64 s[12:13], exec, s[8:9]
	s_cbranch_execz .LBB0_456
	v_lshrrev_b32_e32 v3, 23, v2
	v_add_u32_e32 v3, 0xffffff88, v3
	v_cmp_lt_u32_e32 vcc, 63, v3
	s_nop 1
	v_cndmask_b32_e32 v4, 0, v145, vcc
	v_add_u32_e32 v3, v4, v3
	v_cmp_lt_u32_e64 s[6:7], 31, v3
	s_nop 1
	v_cndmask_b32_e64 v4, 0, v146, s[6:7]
	v_add_u32_e32 v3, v4, v3
	v_cmp_lt_u32_e64 s[8:9], 31, v3
	s_nop 1
	v_cndmask_b32_e64 v4, 0, v146, s[8:9]
	v_add_u32_e32 v3, v4, v3
	v_and_b32_e32 v4, 0x7fffff, v2
	v_or_b32_e32 v4, 0x800000, v4
	v_mad_u64_u32 v[6:7], s[10:11], v4, s38, 0
	v_mov_b32_e32 v62, v7
	v_mad_u64_u32 v[8:9], s[10:11], v4, s39, v[62:63]
	v_mov_b32_e32 v62, v9
	v_mad_u64_u32 v[10:11], s[10:11], v4, s40, v[62:63]
	v_mov_b32_e32 v62, v11
	v_mad_u64_u32 v[12:13], s[10:11], v4, s41, v[62:63]
	v_mov_b32_e32 v62, v13
	v_mad_u64_u32 v[14:15], s[10:11], v4, s42, v[62:63]
	v_mov_b32_e32 v62, v15
	v_mad_u64_u32 v[18:19], s[10:11], v4, s43, v[62:63]
	v_mov_b32_e32 v62, v19
	v_mad_u64_u32 v[20:21], s[10:11], v4, s44, v[62:63]
	v_cndmask_b32_e32 v7, v18, v12, vcc
	v_cndmask_b32_e32 v4, v20, v14, vcc
	v_cndmask_b32_e32 v11, v21, v18, vcc
	v_cndmask_b32_e64 v9, v4, v7, s[6:7]
	v_cndmask_b32_e64 v4, v11, v4, s[6:7]
	v_cndmask_b32_e32 v11, v14, v10, vcc
	v_cndmask_b32_e64 v7, v7, v11, s[6:7]
	v_sub_u32_e32 v13, 32, v3
	v_cmp_eq_u32_e64 s[10:11], 0, v3
	v_cndmask_b32_e32 v3, v12, v8, vcc
	v_cndmask_b32_e64 v4, v4, v9, s[8:9]
	v_cndmask_b32_e64 v9, v9, v7, s[8:9]
	v_cndmask_b32_e64 v8, v11, v3, s[6:7]
	v_alignbit_b32 v14, v4, v9, v13
	v_cndmask_b32_e64 v7, v7, v8, s[8:9]
	v_cndmask_b32_e64 v4, v14, v4, s[10:11]
	v_alignbit_b32 v11, v9, v7, v13
	v_cndmask_b32_e32 v6, v10, v6, vcc
	v_cndmask_b32_e64 v9, v11, v9, s[10:11]
	v_bfe_u32 v14, v4, 29, 1
	v_cndmask_b32_e64 v3, v3, v6, s[6:7]
	v_alignbit_b32 v11, v4, v9, 30
	v_sub_u32_e32 v15, 0, v14
	v_cndmask_b32_e64 v3, v8, v3, s[8:9]
	v_xor_b32_e32 v11, v11, v15
	v_alignbit_b32 v6, v7, v3, v13
	v_cndmask_b32_e64 v6, v6, v7, s[10:11]
	v_ffbh_u32_e32 v8, v11
	v_alignbit_b32 v7, v9, v6, 30
	v_min_u32_e32 v8, 32, v8
	v_alignbit_b32 v3, v6, v3, 30
	v_xor_b32_e32 v7, v7, v15
	v_sub_u32_e32 v9, 31, v8
	v_xor_b32_e32 v3, v3, v15
	v_alignbit_b32 v10, v11, v7, v9
	v_alignbit_b32 v3, v7, v3, v9
	v_alignbit_b32 v6, v10, v3, 9
	v_ffbh_u32_e32 v7, v6
	v_min_u32_e32 v7, 32, v7
	v_lshrrev_b32_e32 v12, 29, v4
	v_not_b32_e32 v9, v7
	v_alignbit_b32 v3, v6, v3, v9
	v_lshlrev_b32_e32 v6, 31, v12
	v_or_b32_e32 v9, 0x33000000, v6
	v_add_lshl_u32 v7, v7, v8, 23
	v_lshrrev_b32_e32 v3, 9, v3
	v_sub_u32_e32 v7, v9, v7
	v_or_b32_e32 v6, 0.5, v6
	v_lshlrev_b32_e32 v8, 23, v8
	v_or_b32_e32 v3, v7, v3
	v_lshrrev_b32_e32 v7, 9, v10
	v_sub_u32_e32 v6, v6, v8
	v_or_b32_e32 v6, v7, v6
	v_mul_f32_e32 v7, 0x3fc90fda, v6
	v_fma_f32 v8, v6, s45, -v7
	v_fmac_f32_e32 v8, 0x33a22168, v6
	v_fmac_f32_e32 v8, 0x3fc90fda, v3
	v_lshrrev_b32_e32 v4, 30, v4
	v_add_f32_e32 v3, v7, v8
	v_add_u32_e32 v4, v14, v4
.LBB0_456:
	s_andn2_saveexec_b64 s[6:7], s[12:13]
	v_mul_f32_e64 v3, |v1|, s46
	v_rndne_f32_e32 v6, v3
	v_cvt_i32_f32_e32 v4, v6
	v_fma_f32 v3, v6, s47, |v1|
	v_fmac_f32_e32 v3, 0xb3a22168, v6
	v_fmac_f32_e32 v3, 0xa7c234c4, v6
	s_or_b64 exec, exec, s[6:7]
	v_mov_b32_e32 v6, v251
	v_mul_f32_e32 v7, v3, v3
	v_and_b32_e32 v8, 1, v4
	v_lshlrev_b32_e32 v4, 30, v4
	v_fmamk_f32 v9, v7, 0xb94c1982, v125
	v_fmamk_f32 v10, v7, 0x37d75334, v143
	v_xor_b32_e32 v2, v2, v1
	v_and_b32_e32 v4, 0x80000000, v4
	v_fmaak_f32 v9, v7, v9, 0xbe2aaa9d
	v_fmaak_f32 v10, v7, v10, 0x3d2aabf7
	v_xor_b32_e32 v2, v2, v4
	v_mul_f32_e32 v4, v7, v9
	v_fmaak_f32 v9, v7, v10, 0xbf000004
	v_fmac_f32_e32 v3, v3, v4
	v_fma_f32 v4, v7, v9, 1.0
	v_cmp_eq_u32_e32 vcc, 0, v8
	s_nop 1
	v_cndmask_b32_e32 v3, v4, v3, vcc
	v_xor_b32_e32 v2, v2, v3
	v_cmp_class_f32_e64 vcc, v1, s49
	s_nop 1
	v_cndmask_b32_e32 v1, v147, v2, vcc
	ds_write_b32 v134, v1 offset:25880
	s_waitcnt vmcnt(0)
	v_mul_f32_e32 v1, v5, v6
	v_and_b32_e32 v2, 0x7fffffff, v1
	v_cmp_nlt_f32_e64 s[6:7], |v1|, s37
	s_and_saveexec_b64 s[8:9], s[6:7]
	s_xor_b64 s[12:13], exec, s[8:9]
	s_cbranch_execz .LBB0_460
	v_lshrrev_b32_e32 v3, 23, v2
	v_add_u32_e32 v3, 0xffffff88, v3
	v_cmp_lt_u32_e32 vcc, 63, v3
	s_nop 1
	v_cndmask_b32_e32 v4, 0, v145, vcc
	v_add_u32_e32 v3, v4, v3
	v_cmp_lt_u32_e64 s[6:7], 31, v3
	s_nop 1
	v_cndmask_b32_e64 v4, 0, v146, s[6:7]
	v_add_u32_e32 v3, v4, v3
	v_cmp_lt_u32_e64 s[8:9], 31, v3
	s_nop 1
	v_cndmask_b32_e64 v4, 0, v146, s[8:9]
	v_add_u32_e32 v3, v4, v3
	v_and_b32_e32 v4, 0x7fffff, v2
	v_or_b32_e32 v16, 0x800000, v4
	v_mad_u64_u32 v[4:5], s[10:11], v16, s38, 0
	v_mov_b32_e32 v62, v5
	v_mad_u64_u32 v[6:7], s[10:11], v16, s39, v[62:63]
	v_mov_b32_e32 v62, v7
	v_mad_u64_u32 v[8:9], s[10:11], v16, s40, v[62:63]
	v_mov_b32_e32 v62, v9
	v_mad_u64_u32 v[10:11], s[10:11], v16, s41, v[62:63]
	v_mov_b32_e32 v62, v11
	v_mad_u64_u32 v[12:13], s[10:11], v16, s42, v[62:63]
	v_mov_b32_e32 v62, v13
	v_mad_u64_u32 v[14:15], s[10:11], v16, s43, v[62:63]
	v_mov_b32_e32 v62, v15
	v_mad_u64_u32 v[18:19], s[10:11], v16, s44, v[62:63]
	v_cndmask_b32_e32 v5, v14, v10, vcc
	v_cndmask_b32_e32 v7, v18, v12, vcc
	v_cndmask_b32_e32 v11, v19, v14, vcc
	v_cndmask_b32_e64 v9, v7, v5, s[6:7]
	v_cndmask_b32_e64 v7, v11, v7, s[6:7]
	v_cndmask_b32_e32 v11, v12, v8, vcc
	v_cndmask_b32_e64 v5, v5, v11, s[6:7]
	v_cndmask_b32_e64 v7, v7, v9, s[8:9]
	v_cndmask_b32_e64 v9, v9, v5, s[8:9]
	v_sub_u32_e32 v12, 32, v3
	v_alignbit_b32 v13, v7, v9, v12
	v_cmp_eq_u32_e64 s[10:11], 0, v3
	v_cndmask_b32_e32 v6, v10, v6, vcc
	v_cndmask_b32_e32 v4, v8, v4, vcc
	v_cndmask_b32_e64 v3, v13, v7, s[10:11]
	v_cndmask_b32_e64 v7, v11, v6, s[6:7]
	v_cndmask_b32_e64 v5, v5, v7, s[8:9]
	v_alignbit_b32 v10, v9, v5, v12
	v_cndmask_b32_e64 v9, v10, v9, s[10:11]
	v_bfe_u32 v13, v3, 29, 1
	v_cndmask_b32_e64 v4, v6, v4, s[6:7]
	v_alignbit_b32 v10, v3, v9, 30
	v_sub_u32_e32 v14, 0, v13
	v_cndmask_b32_e64 v4, v7, v4, s[8:9]
	v_xor_b32_e32 v10, v10, v14
	v_alignbit_b32 v6, v5, v4, v12
	v_cndmask_b32_e64 v5, v6, v5, s[10:11]
	v_ffbh_u32_e32 v7, v10
	v_alignbit_b32 v6, v9, v5, 30
	v_min_u32_e32 v7, 32, v7
	v_alignbit_b32 v4, v5, v4, 30
	v_xor_b32_e32 v6, v6, v14
	v_sub_u32_e32 v8, 31, v7
	v_xor_b32_e32 v4, v4, v14
	v_alignbit_b32 v9, v10, v6, v8
	v_alignbit_b32 v4, v6, v4, v8
	v_alignbit_b32 v5, v9, v4, 9
	v_ffbh_u32_e32 v6, v5
	v_min_u32_e32 v6, 32, v6
	v_lshrrev_b32_e32 v11, 29, v3
	v_not_b32_e32 v8, v6
	v_alignbit_b32 v4, v5, v4, v8
	v_lshlrev_b32_e32 v5, 31, v11
	v_or_b32_e32 v8, 0x33000000, v5
	v_add_lshl_u32 v6, v6, v7, 23
	v_lshrrev_b32_e32 v4, 9, v4
	v_sub_u32_e32 v6, v8, v6
	v_or_b32_e32 v5, 0.5, v5
	v_lshlrev_b32_e32 v7, 23, v7
	v_or_b32_e32 v4, v6, v4
	v_lshrrev_b32_e32 v6, 9, v9
	v_sub_u32_e32 v5, v5, v7
	v_or_b32_e32 v5, v6, v5
	v_mul_f32_e32 v6, 0x3fc90fda, v5
	v_fma_f32 v7, v5, s45, -v6
	v_fmac_f32_e32 v7, 0x33a22168, v5
	v_fmac_f32_e32 v7, 0x3fc90fda, v4
	v_lshrrev_b32_e32 v3, 30, v3
	v_add_f32_e32 v4, v6, v7
	v_add_u32_e32 v3, v13, v3
